# P11 top-256: hand-written SGPR threshold descent (v_cmp+v_addc counting) and v_writelane mask build in front of the compiler code; ties fall back to the original path
# speedup vs baseline: 1.0107x; 1.0107x over previous
.LBB0_1617:
	s_lshl_b64 s[0:1], s[0:1], 8
	v_readlane_b32 s4, v253, 13
	s_waitcnt lgkmcnt(0)
	v_readlane_b32 s5, v253, 14
	s_add_u32 s0, s4, s0
	s_barrier
	s_addc_u32 s1, s5, s1
	v_writelane_b32 v252, s0, 49
	s_and_b64 vcc, exec, s[26:27]
	v_writelane_b32 v254, s26, 35
	v_writelane_b32 v252, s1, 50
	s_nop 0
	v_writelane_b32 v254, s27, 36
	s_cmp_lt_u32 s33, 4
	s_cbranch_scc1 .Ltk0_orig
	s_mov_b32 s4, 0
	s_mov_b32 s5, 0x80000000
	s_cmp_lt_u32 s33, 8
	s_cbranch_scc1 .Ltk0_l8
	s_cmp_lt_u32 s33, 16
	s_cbranch_scc1 .Ltk0_l16
	s_cmp_lt_u32 s33, 24
	s_cbranch_scc1 .Ltk0_l24
.Ltk0_l32:
	s_or_b32 s6, s4, s5
	v_cmp_le_u32_e64 s[8:9], s6, v172
	v_cmp_le_u32_e64 s[12:13], s6, v179
	v_cmp_le_u32_e64 s[16:17], s6, v181
	v_cndmask_b32_e64 v8, 0, 1, s[8:9]
	v_cmp_le_u32_e64 s[8:9], s6, v183
	v_addc_co_u32_e64 v8, s[20:21], 0, v8, s[12:13]
	v_cmp_le_u32_e64 s[12:13], s6, v185
	v_addc_co_u32_e64 v8, s[20:21], 0, v8, s[16:17]
	v_cmp_le_u32_e64 s[16:17], s6, v187
	v_addc_co_u32_e64 v8, s[20:21], 0, v8, s[8:9]
	v_cmp_le_u32_e64 s[8:9], s6, v189
	v_addc_co_u32_e64 v8, s[20:21], 0, v8, s[12:13]
	v_cmp_le_u32_e64 s[12:13], s6, v190
	v_addc_co_u32_e64 v8, s[20:21], 0, v8, s[16:17]
	v_cmp_le_u32_e64 s[16:17], s6, v191
	v_addc_co_u32_e64 v8, s[20:21], 0, v8, s[8:9]
	v_cmp_le_u32_e64 s[8:9], s6, v192
	v_addc_co_u32_e64 v8, s[20:21], 0, v8, s[12:13]
	v_cmp_le_u32_e64 s[12:13], s6, v193
	v_addc_co_u32_e64 v8, s[20:21], 0, v8, s[16:17]
	v_cmp_le_u32_e64 s[16:17], s6, v194
	v_addc_co_u32_e64 v8, s[20:21], 0, v8, s[8:9]
	v_cmp_le_u32_e64 s[8:9], s6, v195
	v_addc_co_u32_e64 v8, s[20:21], 0, v8, s[12:13]
	v_cmp_le_u32_e64 s[12:13], s6, v196
	v_addc_co_u32_e64 v8, s[20:21], 0, v8, s[16:17]
	v_cmp_le_u32_e64 s[16:17], s6, v198
	v_addc_co_u32_e64 v8, s[20:21], 0, v8, s[8:9]
	v_cmp_le_u32_e64 s[8:9], s6, v200
	v_addc_co_u32_e64 v8, s[20:21], 0, v8, s[12:13]
	v_cmp_le_u32_e64 s[12:13], s6, v206
	v_addc_co_u32_e64 v8, s[20:21], 0, v8, s[16:17]
	v_cmp_le_u32_e64 s[16:17], s6, v207
	v_addc_co_u32_e64 v8, s[20:21], 0, v8, s[8:9]
	v_cmp_le_u32_e64 s[8:9], s6, v208
	v_addc_co_u32_e64 v8, s[20:21], 0, v8, s[12:13]
	v_cmp_le_u32_e64 s[12:13], s6, v209
	v_addc_co_u32_e64 v8, s[20:21], 0, v8, s[16:17]
	v_cmp_le_u32_e64 s[16:17], s6, v210
	v_addc_co_u32_e64 v8, s[20:21], 0, v8, s[8:9]
	v_cmp_le_u32_e64 s[8:9], s6, v211
	v_addc_co_u32_e64 v8, s[20:21], 0, v8, s[12:13]
	v_cmp_le_u32_e64 s[12:13], s6, v212
	v_addc_co_u32_e64 v8, s[20:21], 0, v8, s[16:17]
	v_cmp_le_u32_e64 s[16:17], s6, v213
	v_addc_co_u32_e64 v8, s[20:21], 0, v8, s[8:9]
	v_cmp_le_u32_e64 s[8:9], s6, v214
	v_addc_co_u32_e64 v8, s[20:21], 0, v8, s[12:13]
	v_cmp_le_u32_e64 s[12:13], s6, v215
	v_addc_co_u32_e64 v8, s[20:21], 0, v8, s[16:17]
	v_cmp_le_u32_e64 s[16:17], s6, v216
	v_addc_co_u32_e64 v8, s[20:21], 0, v8, s[8:9]
	v_cmp_le_u32_e64 s[8:9], s6, v217
	v_addc_co_u32_e64 v8, s[20:21], 0, v8, s[12:13]
	v_cmp_le_u32_e64 s[12:13], s6, v219
	v_addc_co_u32_e64 v8, s[20:21], 0, v8, s[16:17]
	v_cmp_le_u32_e64 s[16:17], s6, v220
	v_addc_co_u32_e64 v8, s[20:21], 0, v8, s[8:9]
	v_cmp_le_u32_e64 s[8:9], s6, v221
	v_addc_co_u32_e64 v8, s[20:21], 0, v8, s[12:13]
	v_cmp_le_u32_e64 s[12:13], s6, v2
	v_addc_co_u32_e64 v8, s[20:21], 0, v8, s[16:17]
	v_addc_co_u32_e64 v8, s[20:21], 0, v8, s[8:9]
	v_addc_co_u32_e64 v8, s[20:21], 0, v8, s[12:13]
	v_and_b32_e32 v9, 32, v8
	v_cmp_ne_u32_e64 s[0:1], 0, v9
	v_and_b32_e32 v9, 16, v8
	v_cmp_ne_u32_e64 s[22:23], 0, v9
	v_and_b32_e32 v9, 8, v8
	v_cmp_ne_u32_e64 s[18:19], 0, v9
	v_and_b32_e32 v9, 4, v8
	v_cmp_ne_u32_e64 s[16:17], 0, v9
	v_and_b32_e32 v9, 2, v8
	v_cmp_ne_u32_e64 s[12:13], 0, v9
	v_and_b32_e32 v9, 1, v8
	v_cmp_ne_u32_e64 s[8:9], 0, v9
	s_bcnt1_i32_b64 s7, s[0:1]
	s_bcnt1_i32_b64 s3, s[22:23]
	s_lshl1_add_u32 s7, s7, s3
	s_bcnt1_i32_b64 s3, s[18:19]
	s_lshl1_add_u32 s7, s7, s3
	s_bcnt1_i32_b64 s3, s[16:17]
	s_lshl1_add_u32 s7, s7, s3
	s_bcnt1_i32_b64 s3, s[12:13]
	s_lshl1_add_u32 s7, s7, s3
	s_bcnt1_i32_b64 s3, s[8:9]
	s_lshl1_add_u32 s7, s7, s3
	s_cmpk_lt_u32 s7, 0x100
	s_cselect_b32 s4, s4, s6
	s_cmpk_eq_u32 s7, 0x100
	s_cbranch_scc1 .Ltk0_x32
	s_lshr_b32 s5, s5, 1
	s_cbranch_scc1 .Ltk0_l32
	s_branch .Ltk0_orig
.Ltk0_l24:
	s_or_b32 s6, s4, s5
	v_cmp_le_u32_e64 s[8:9], s6, v172
	v_cmp_le_u32_e64 s[12:13], s6, v179
	v_cmp_le_u32_e64 s[16:17], s6, v181
	v_cndmask_b32_e64 v8, 0, 1, s[8:9]
	v_cmp_le_u32_e64 s[8:9], s6, v183
	v_addc_co_u32_e64 v8, s[20:21], 0, v8, s[12:13]
	v_cmp_le_u32_e64 s[12:13], s6, v185
	v_addc_co_u32_e64 v8, s[20:21], 0, v8, s[16:17]
	v_cmp_le_u32_e64 s[16:17], s6, v187
	v_addc_co_u32_e64 v8, s[20:21], 0, v8, s[8:9]
	v_cmp_le_u32_e64 s[8:9], s6, v189
	v_addc_co_u32_e64 v8, s[20:21], 0, v8, s[12:13]
	v_cmp_le_u32_e64 s[12:13], s6, v190
	v_addc_co_u32_e64 v8, s[20:21], 0, v8, s[16:17]
	v_cmp_le_u32_e64 s[16:17], s6, v191
	v_addc_co_u32_e64 v8, s[20:21], 0, v8, s[8:9]
	v_cmp_le_u32_e64 s[8:9], s6, v192
	v_addc_co_u32_e64 v8, s[20:21], 0, v8, s[12:13]
	v_cmp_le_u32_e64 s[12:13], s6, v193
	v_addc_co_u32_e64 v8, s[20:21], 0, v8, s[16:17]
	v_cmp_le_u32_e64 s[16:17], s6, v194
	v_addc_co_u32_e64 v8, s[20:21], 0, v8, s[8:9]
	v_cmp_le_u32_e64 s[8:9], s6, v195
	v_addc_co_u32_e64 v8, s[20:21], 0, v8, s[12:13]
	v_cmp_le_u32_e64 s[12:13], s6, v196
	v_addc_co_u32_e64 v8, s[20:21], 0, v8, s[16:17]
	v_cmp_le_u32_e64 s[16:17], s6, v198
	v_addc_co_u32_e64 v8, s[20:21], 0, v8, s[8:9]
	v_cmp_le_u32_e64 s[8:9], s6, v200
	v_addc_co_u32_e64 v8, s[20:21], 0, v8, s[12:13]
	v_cmp_le_u32_e64 s[12:13], s6, v206
	v_addc_co_u32_e64 v8, s[20:21], 0, v8, s[16:17]
	v_cmp_le_u32_e64 s[16:17], s6, v207
	v_addc_co_u32_e64 v8, s[20:21], 0, v8, s[8:9]
	v_cmp_le_u32_e64 s[8:9], s6, v208
	v_addc_co_u32_e64 v8, s[20:21], 0, v8, s[12:13]
	v_cmp_le_u32_e64 s[12:13], s6, v209
	v_addc_co_u32_e64 v8, s[20:21], 0, v8, s[16:17]
	v_cmp_le_u32_e64 s[16:17], s6, v210
	v_addc_co_u32_e64 v8, s[20:21], 0, v8, s[8:9]
	v_cmp_le_u32_e64 s[8:9], s6, v211
	v_addc_co_u32_e64 v8, s[20:21], 0, v8, s[12:13]
	v_cmp_le_u32_e64 s[12:13], s6, v212
	v_addc_co_u32_e64 v8, s[20:21], 0, v8, s[16:17]
	v_cmp_le_u32_e64 s[16:17], s6, v213
	v_addc_co_u32_e64 v8, s[20:21], 0, v8, s[8:9]
	v_addc_co_u32_e64 v8, s[20:21], 0, v8, s[12:13]
	v_addc_co_u32_e64 v8, s[20:21], 0, v8, s[16:17]
	v_and_b32_e32 v9, 16, v8
	v_cmp_ne_u32_e64 s[22:23], 0, v9
	v_and_b32_e32 v9, 8, v8
	v_cmp_ne_u32_e64 s[18:19], 0, v9
	v_and_b32_e32 v9, 4, v8
	v_cmp_ne_u32_e64 s[16:17], 0, v9
	v_and_b32_e32 v9, 2, v8
	v_cmp_ne_u32_e64 s[12:13], 0, v9
	v_and_b32_e32 v9, 1, v8
	v_cmp_ne_u32_e64 s[8:9], 0, v9
	s_bcnt1_i32_b64 s7, s[22:23]
	s_bcnt1_i32_b64 s3, s[18:19]
	s_lshl1_add_u32 s7, s7, s3
	s_bcnt1_i32_b64 s3, s[16:17]
	s_lshl1_add_u32 s7, s7, s3
	s_bcnt1_i32_b64 s3, s[12:13]
	s_lshl1_add_u32 s7, s7, s3
	s_bcnt1_i32_b64 s3, s[8:9]
	s_lshl1_add_u32 s7, s7, s3
	s_cmpk_lt_u32 s7, 0x100
	s_cselect_b32 s4, s4, s6
	s_cmpk_eq_u32 s7, 0x100
	s_cbranch_scc1 .Ltk0_x24
	s_lshr_b32 s5, s5, 1
	s_cbranch_scc1 .Ltk0_l24
	s_branch .Ltk0_orig
.Ltk0_l16:
	s_or_b32 s6, s4, s5
	v_cmp_le_u32_e64 s[8:9], s6, v172
	v_cmp_le_u32_e64 s[12:13], s6, v179
	v_cmp_le_u32_e64 s[16:17], s6, v181
	v_cndmask_b32_e64 v8, 0, 1, s[8:9]
	v_cmp_le_u32_e64 s[8:9], s6, v183
	v_addc_co_u32_e64 v8, s[20:21], 0, v8, s[12:13]
	v_cmp_le_u32_e64 s[12:13], s6, v185
	v_addc_co_u32_e64 v8, s[20:21], 0, v8, s[16:17]
	v_cmp_le_u32_e64 s[16:17], s6, v187
	v_addc_co_u32_e64 v8, s[20:21], 0, v8, s[8:9]
	v_cmp_le_u32_e64 s[8:9], s6, v189
	v_addc_co_u32_e64 v8, s[20:21], 0, v8, s[12:13]
	v_cmp_le_u32_e64 s[12:13], s6, v190
	v_addc_co_u32_e64 v8, s[20:21], 0, v8, s[16:17]
	v_cmp_le_u32_e64 s[16:17], s6, v191
	v_addc_co_u32_e64 v8, s[20:21], 0, v8, s[8:9]
	v_cmp_le_u32_e64 s[8:9], s6, v192
	v_addc_co_u32_e64 v8, s[20:21], 0, v8, s[12:13]
	v_cmp_le_u32_e64 s[12:13], s6, v193
	v_addc_co_u32_e64 v8, s[20:21], 0, v8, s[16:17]
	v_cmp_le_u32_e64 s[16:17], s6, v194
	v_addc_co_u32_e64 v8, s[20:21], 0, v8, s[8:9]
	v_cmp_le_u32_e64 s[8:9], s6, v195
	v_addc_co_u32_e64 v8, s[20:21], 0, v8, s[12:13]
	v_cmp_le_u32_e64 s[12:13], s6, v196
	v_addc_co_u32_e64 v8, s[20:21], 0, v8, s[16:17]
	v_cmp_le_u32_e64 s[16:17], s6, v198
	v_addc_co_u32_e64 v8, s[20:21], 0, v8, s[8:9]
	v_cmp_le_u32_e64 s[8:9], s6, v200
	v_addc_co_u32_e64 v8, s[20:21], 0, v8, s[12:13]
	v_addc_co_u32_e64 v8, s[20:21], 0, v8, s[16:17]
	v_addc_co_u32_e64 v8, s[20:21], 0, v8, s[8:9]
	v_and_b32_e32 v9, 16, v8
	v_cmp_ne_u32_e64 s[22:23], 0, v9
	v_and_b32_e32 v9, 8, v8
	v_cmp_ne_u32_e64 s[18:19], 0, v9
	v_and_b32_e32 v9, 4, v8
	v_cmp_ne_u32_e64 s[16:17], 0, v9
	v_and_b32_e32 v9, 2, v8
	v_cmp_ne_u32_e64 s[12:13], 0, v9
	v_and_b32_e32 v9, 1, v8
	v_cmp_ne_u32_e64 s[8:9], 0, v9
	s_bcnt1_i32_b64 s7, s[22:23]
	s_bcnt1_i32_b64 s3, s[18:19]
	s_lshl1_add_u32 s7, s7, s3
	s_bcnt1_i32_b64 s3, s[16:17]
	s_lshl1_add_u32 s7, s7, s3
	s_bcnt1_i32_b64 s3, s[12:13]
	s_lshl1_add_u32 s7, s7, s3
	s_bcnt1_i32_b64 s3, s[8:9]
	s_lshl1_add_u32 s7, s7, s3
	s_cmpk_lt_u32 s7, 0x100
	s_cselect_b32 s4, s4, s6
	s_cmpk_eq_u32 s7, 0x100
	s_cbranch_scc1 .Ltk0_x16
	s_lshr_b32 s5, s5, 1
	s_cbranch_scc1 .Ltk0_l16
	s_branch .Ltk0_orig
.Ltk0_l8:
	s_or_b32 s6, s4, s5
	v_cmp_le_u32_e64 s[8:9], s6, v172
	v_cmp_le_u32_e64 s[12:13], s6, v179
	v_cmp_le_u32_e64 s[16:17], s6, v181
	v_cndmask_b32_e64 v8, 0, 1, s[8:9]
	v_cmp_le_u32_e64 s[8:9], s6, v183
	v_addc_co_u32_e64 v8, s[20:21], 0, v8, s[12:13]
	v_cmp_le_u32_e64 s[12:13], s6, v185
	v_addc_co_u32_e64 v8, s[20:21], 0, v8, s[16:17]
	v_cmp_le_u32_e64 s[16:17], s6, v187
	v_addc_co_u32_e64 v8, s[20:21], 0, v8, s[8:9]
	v_cmp_le_u32_e64 s[8:9], s6, v189
	v_addc_co_u32_e64 v8, s[20:21], 0, v8, s[12:13]
	v_cmp_le_u32_e64 s[12:13], s6, v190
	v_addc_co_u32_e64 v8, s[20:21], 0, v8, s[16:17]
	v_addc_co_u32_e64 v8, s[20:21], 0, v8, s[8:9]
	v_addc_co_u32_e64 v8, s[20:21], 0, v8, s[12:13]
	v_and_b32_e32 v9, 8, v8
	v_cmp_ne_u32_e64 s[18:19], 0, v9
	v_and_b32_e32 v9, 4, v8
	v_cmp_ne_u32_e64 s[16:17], 0, v9
	v_and_b32_e32 v9, 2, v8
	v_cmp_ne_u32_e64 s[12:13], 0, v9
	v_and_b32_e32 v9, 1, v8
	v_cmp_ne_u32_e64 s[8:9], 0, v9
	s_bcnt1_i32_b64 s7, s[18:19]
	s_bcnt1_i32_b64 s3, s[16:17]
	s_lshl1_add_u32 s7, s7, s3
	s_bcnt1_i32_b64 s3, s[12:13]
	s_lshl1_add_u32 s7, s7, s3
	s_bcnt1_i32_b64 s3, s[8:9]
	s_lshl1_add_u32 s7, s7, s3
	s_cmpk_lt_u32 s7, 0x100
	s_cselect_b32 s4, s4, s6
	s_cmpk_eq_u32 s7, 0x100
	s_cbranch_scc1 .Ltk0_x8
	s_lshr_b32 s5, s5, 1
	s_cbranch_scc1 .Ltk0_l8
	s_branch .Ltk0_orig
.Ltk0_x32:
	v_cmp_le_u32_e64 s[8:9], s4, v172
	v_cmp_le_u32_e64 s[12:13], s4, v179
	v_cmp_le_u32_e64 s[16:17], s4, v181
	s_nop 0
	v_writelane_b32 v10, s8, 0
	v_writelane_b32 v11, s9, 0
	v_cmp_le_u32_e64 s[8:9], s4, v183
	v_writelane_b32 v10, s12, 1
	v_writelane_b32 v11, s13, 1
	v_cmp_le_u32_e64 s[12:13], s4, v185
	v_writelane_b32 v10, s16, 2
	v_writelane_b32 v11, s17, 2
	v_cmp_le_u32_e64 s[16:17], s4, v187
	v_writelane_b32 v10, s8, 3
	v_writelane_b32 v11, s9, 3
	v_cmp_le_u32_e64 s[8:9], s4, v189
	v_writelane_b32 v10, s12, 4
	v_writelane_b32 v11, s13, 4
	v_cmp_le_u32_e64 s[12:13], s4, v190
	v_writelane_b32 v10, s16, 5
	v_writelane_b32 v11, s17, 5
	v_cmp_le_u32_e64 s[16:17], s4, v191
	v_writelane_b32 v10, s8, 6
	v_writelane_b32 v11, s9, 6
	v_cmp_le_u32_e64 s[8:9], s4, v192
	v_writelane_b32 v10, s12, 7
	v_writelane_b32 v11, s13, 7
	v_cmp_le_u32_e64 s[12:13], s4, v193
	v_writelane_b32 v10, s16, 8
	v_writelane_b32 v11, s17, 8
	v_cmp_le_u32_e64 s[16:17], s4, v194
	v_writelane_b32 v10, s8, 9
	v_writelane_b32 v11, s9, 9
	v_cmp_le_u32_e64 s[8:9], s4, v195
	v_writelane_b32 v10, s12, 10
	v_writelane_b32 v11, s13, 10
	v_cmp_le_u32_e64 s[12:13], s4, v196
	v_writelane_b32 v10, s16, 11
	v_writelane_b32 v11, s17, 11
	v_cmp_le_u32_e64 s[16:17], s4, v198
	v_writelane_b32 v10, s8, 12
	v_writelane_b32 v11, s9, 12
	v_cmp_le_u32_e64 s[8:9], s4, v200
	v_writelane_b32 v10, s12, 13
	v_writelane_b32 v11, s13, 13
	v_cmp_le_u32_e64 s[12:13], s4, v206
	v_writelane_b32 v10, s16, 14
	v_writelane_b32 v11, s17, 14
	v_cmp_le_u32_e64 s[16:17], s4, v207
	v_writelane_b32 v10, s8, 15
	v_writelane_b32 v11, s9, 15
	v_cmp_le_u32_e64 s[8:9], s4, v208
	v_writelane_b32 v10, s12, 16
	v_writelane_b32 v11, s13, 16
	v_cmp_le_u32_e64 s[12:13], s4, v209
	v_writelane_b32 v10, s16, 17
	v_writelane_b32 v11, s17, 17
	v_cmp_le_u32_e64 s[16:17], s4, v210
	v_writelane_b32 v10, s8, 18
	v_writelane_b32 v11, s9, 18
	v_cmp_le_u32_e64 s[8:9], s4, v211
	v_writelane_b32 v10, s12, 19
	v_writelane_b32 v11, s13, 19
	v_cmp_le_u32_e64 s[12:13], s4, v212
	v_writelane_b32 v10, s16, 20
	v_writelane_b32 v11, s17, 20
	v_cmp_le_u32_e64 s[16:17], s4, v213
	v_writelane_b32 v10, s8, 21
	v_writelane_b32 v11, s9, 21
	v_cmp_le_u32_e64 s[8:9], s4, v214
	v_writelane_b32 v10, s12, 22
	v_writelane_b32 v11, s13, 22
	v_cmp_le_u32_e64 s[12:13], s4, v215
	v_writelane_b32 v10, s16, 23
	v_writelane_b32 v11, s17, 23
	v_cmp_le_u32_e64 s[16:17], s4, v216
	v_writelane_b32 v10, s8, 24
	v_writelane_b32 v11, s9, 24
	v_cmp_le_u32_e64 s[8:9], s4, v217
	v_writelane_b32 v10, s12, 25
	v_writelane_b32 v11, s13, 25
	v_cmp_le_u32_e64 s[12:13], s4, v219
	v_writelane_b32 v10, s16, 26
	v_writelane_b32 v11, s17, 26
	v_cmp_le_u32_e64 s[16:17], s4, v220
	v_writelane_b32 v10, s8, 27
	v_writelane_b32 v11, s9, 27
	v_cmp_le_u32_e64 s[8:9], s4, v221
	v_writelane_b32 v10, s12, 28
	v_writelane_b32 v11, s13, 28
	v_cmp_le_u32_e64 s[12:13], s4, v2
	v_writelane_b32 v10, s16, 29
	v_writelane_b32 v11, s17, 29
	v_writelane_b32 v10, s8, 30
	v_writelane_b32 v11, s9, 30
	v_writelane_b32 v10, s12, 31
	v_writelane_b32 v11, s13, 31
	v_mov_b32_e32 v2, v10
	v_mov_b32_e32 v3, v11
	s_branch .LBB0_1883
.Ltk0_x24:
	v_cmp_le_u32_e64 s[8:9], s4, v172
	v_cmp_le_u32_e64 s[12:13], s4, v179
	v_cmp_le_u32_e64 s[16:17], s4, v181
	s_nop 0
	v_writelane_b32 v10, s8, 0
	v_writelane_b32 v11, s9, 0
	v_cmp_le_u32_e64 s[8:9], s4, v183
	v_writelane_b32 v10, s12, 1
	v_writelane_b32 v11, s13, 1
	v_cmp_le_u32_e64 s[12:13], s4, v185
	v_writelane_b32 v10, s16, 2
	v_writelane_b32 v11, s17, 2
	v_cmp_le_u32_e64 s[16:17], s4, v187
	v_writelane_b32 v10, s8, 3
	v_writelane_b32 v11, s9, 3
	v_cmp_le_u32_e64 s[8:9], s4, v189
	v_writelane_b32 v10, s12, 4
	v_writelane_b32 v11, s13, 4
	v_cmp_le_u32_e64 s[12:13], s4, v190
	v_writelane_b32 v10, s16, 5
	v_writelane_b32 v11, s17, 5
	v_cmp_le_u32_e64 s[16:17], s4, v191
	v_writelane_b32 v10, s8, 6
	v_writelane_b32 v11, s9, 6
	v_cmp_le_u32_e64 s[8:9], s4, v192
	v_writelane_b32 v10, s12, 7
	v_writelane_b32 v11, s13, 7
	v_cmp_le_u32_e64 s[12:13], s4, v193
	v_writelane_b32 v10, s16, 8
	v_writelane_b32 v11, s17, 8
	v_cmp_le_u32_e64 s[16:17], s4, v194
	v_writelane_b32 v10, s8, 9
	v_writelane_b32 v11, s9, 9
	v_cmp_le_u32_e64 s[8:9], s4, v195
	v_writelane_b32 v10, s12, 10
	v_writelane_b32 v11, s13, 10
	v_cmp_le_u32_e64 s[12:13], s4, v196
	v_writelane_b32 v10, s16, 11
	v_writelane_b32 v11, s17, 11
	v_cmp_le_u32_e64 s[16:17], s4, v198
	v_writelane_b32 v10, s8, 12
	v_writelane_b32 v11, s9, 12
	v_cmp_le_u32_e64 s[8:9], s4, v200
	v_writelane_b32 v10, s12, 13
	v_writelane_b32 v11, s13, 13
	v_cmp_le_u32_e64 s[12:13], s4, v206
	v_writelane_b32 v10, s16, 14
	v_writelane_b32 v11, s17, 14
	v_cmp_le_u32_e64 s[16:17], s4, v207
	v_writelane_b32 v10, s8, 15
	v_writelane_b32 v11, s9, 15
	v_cmp_le_u32_e64 s[8:9], s4, v208
	v_writelane_b32 v10, s12, 16
	v_writelane_b32 v11, s13, 16
	v_cmp_le_u32_e64 s[12:13], s4, v209
	v_writelane_b32 v10, s16, 17
	v_writelane_b32 v11, s17, 17
	v_cmp_le_u32_e64 s[16:17], s4, v210
	v_writelane_b32 v10, s8, 18
	v_writelane_b32 v11, s9, 18
	v_cmp_le_u32_e64 s[8:9], s4, v211
	v_writelane_b32 v10, s12, 19
	v_writelane_b32 v11, s13, 19
	v_cmp_le_u32_e64 s[12:13], s4, v212
	v_writelane_b32 v10, s16, 20
	v_writelane_b32 v11, s17, 20
	v_cmp_le_u32_e64 s[16:17], s4, v213
	v_writelane_b32 v10, s8, 21
	v_writelane_b32 v11, s9, 21
	v_writelane_b32 v10, s12, 22
	v_writelane_b32 v11, s13, 22
	v_writelane_b32 v10, s16, 23
	v_writelane_b32 v11, s17, 23
	v_mov_b32_e32 v2, v10
	v_mov_b32_e32 v3, v11
	s_branch .LBB0_1883
.Ltk0_x16:
	v_cmp_le_u32_e64 s[8:9], s4, v172
	v_cmp_le_u32_e64 s[12:13], s4, v179
	v_cmp_le_u32_e64 s[16:17], s4, v181
	s_nop 0
	v_writelane_b32 v10, s8, 0
	v_writelane_b32 v11, s9, 0
	v_cmp_le_u32_e64 s[8:9], s4, v183
	v_writelane_b32 v10, s12, 1
	v_writelane_b32 v11, s13, 1
	v_cmp_le_u32_e64 s[12:13], s4, v185
	v_writelane_b32 v10, s16, 2
	v_writelane_b32 v11, s17, 2
	v_cmp_le_u32_e64 s[16:17], s4, v187
	v_writelane_b32 v10, s8, 3
	v_writelane_b32 v11, s9, 3
	v_cmp_le_u32_e64 s[8:9], s4, v189
	v_writelane_b32 v10, s12, 4
	v_writelane_b32 v11, s13, 4
	v_cmp_le_u32_e64 s[12:13], s4, v190
	v_writelane_b32 v10, s16, 5
	v_writelane_b32 v11, s17, 5
	v_cmp_le_u32_e64 s[16:17], s4, v191
	v_writelane_b32 v10, s8, 6
	v_writelane_b32 v11, s9, 6
	v_cmp_le_u32_e64 s[8:9], s4, v192
	v_writelane_b32 v10, s12, 7
	v_writelane_b32 v11, s13, 7
	v_cmp_le_u32_e64 s[12:13], s4, v193
	v_writelane_b32 v10, s16, 8
	v_writelane_b32 v11, s17, 8
	v_cmp_le_u32_e64 s[16:17], s4, v194
	v_writelane_b32 v10, s8, 9
	v_writelane_b32 v11, s9, 9
	v_cmp_le_u32_e64 s[8:9], s4, v195
	v_writelane_b32 v10, s12, 10
	v_writelane_b32 v11, s13, 10
	v_cmp_le_u32_e64 s[12:13], s4, v196
	v_writelane_b32 v10, s16, 11
	v_writelane_b32 v11, s17, 11
	v_cmp_le_u32_e64 s[16:17], s4, v198
	v_writelane_b32 v10, s8, 12
	v_writelane_b32 v11, s9, 12
	v_cmp_le_u32_e64 s[8:9], s4, v200
	v_writelane_b32 v10, s12, 13
	v_writelane_b32 v11, s13, 13
	v_writelane_b32 v10, s16, 14
	v_writelane_b32 v11, s17, 14
	v_writelane_b32 v10, s8, 15
	v_writelane_b32 v11, s9, 15
	v_mov_b32_e32 v2, v10
	v_mov_b32_e32 v3, v11
	s_branch .LBB0_1883
.Ltk0_x8:
	v_cmp_le_u32_e64 s[8:9], s4, v172
	v_cmp_le_u32_e64 s[12:13], s4, v179
	v_cmp_le_u32_e64 s[16:17], s4, v181
	s_nop 0
	v_writelane_b32 v10, s8, 0
	v_writelane_b32 v11, s9, 0
	v_cmp_le_u32_e64 s[8:9], s4, v183
	v_writelane_b32 v10, s12, 1
	v_writelane_b32 v11, s13, 1
	v_cmp_le_u32_e64 s[12:13], s4, v185
	v_writelane_b32 v10, s16, 2
	v_writelane_b32 v11, s17, 2
	v_cmp_le_u32_e64 s[16:17], s4, v187
	v_writelane_b32 v10, s8, 3
	v_writelane_b32 v11, s9, 3
	v_cmp_le_u32_e64 s[8:9], s4, v189
	v_writelane_b32 v10, s12, 4
	v_writelane_b32 v11, s13, 4
	v_cmp_le_u32_e64 s[12:13], s4, v190
	v_writelane_b32 v10, s16, 5
	v_writelane_b32 v11, s17, 5
	v_writelane_b32 v10, s8, 6
	v_writelane_b32 v11, s9, 6
	v_writelane_b32 v10, s12, 7
	v_writelane_b32 v11, s13, 7
	v_mov_b32_e32 v2, v10
	v_mov_b32_e32 v3, v11
	s_branch .LBB0_1883
.Ltk0_orig:
	s_and_b64 vcc, exec, s[26:27]
	s_cbranch_vccz .LBB0_1724
	v_readlane_b32 s0, v252, 55
	v_readlane_b32 s1, v252, 56
	s_and_b64 vcc, exec, s[0:1]
	s_cbranch_vccz .LBB0_1725
	v_readlane_b32 s0, v254, 37
	v_readlane_b32 s1, v254, 38
	s_and_b64 vcc, exec, s[0:1]
	s_cbranch_vccz .LBB0_1726
	v_mov_b32_e32 v5, 31
	v_mov_b32_e32 v3, 0

.LBB0_1886:
	s_or_b64 exec, exec, s[0:1]
	s_cmp_lt_u32 s33, 4
	s_cbranch_scc1 .Ltk1_orig
	s_mov_b32 s4, 0
	s_mov_b32 s5, 0x80000000
	s_cmp_lt_u32 s33, 8
	s_cbranch_scc1 .Ltk1_l8
	s_cmp_lt_u32 s33, 16
	s_cbranch_scc1 .Ltk1_l16
	s_cmp_lt_u32 s33, 24
	s_cbranch_scc1 .Ltk1_l24
.Ltk1_l32:
	s_or_b32 s6, s4, s5
	v_cmp_le_u32_e64 s[8:9], s6, v140
	v_cmp_le_u32_e64 s[12:13], s6, v142
	v_cmp_le_u32_e64 s[16:17], s6, v144
	v_cndmask_b32_e64 v8, 0, 1, s[8:9]
	v_cmp_le_u32_e64 s[8:9], s6, v146
	v_addc_co_u32_e64 v8, s[20:21], 0, v8, s[12:13]
	v_cmp_le_u32_e64 s[12:13], s6, v148
	v_addc_co_u32_e64 v8, s[20:21], 0, v8, s[16:17]
	v_cmp_le_u32_e64 s[16:17], s6, v150
	v_addc_co_u32_e64 v8, s[20:21], 0, v8, s[8:9]
	v_cmp_le_u32_e64 s[8:9], s6, v152
	v_addc_co_u32_e64 v8, s[20:21], 0, v8, s[12:13]
	v_cmp_le_u32_e64 s[12:13], s6, v153
	v_addc_co_u32_e64 v8, s[20:21], 0, v8, s[16:17]
	v_cmp_le_u32_e64 s[16:17], s6, v154
	v_addc_co_u32_e64 v8, s[20:21], 0, v8, s[8:9]
	v_cmp_le_u32_e64 s[8:9], s6, v155
	v_addc_co_u32_e64 v8, s[20:21], 0, v8, s[12:13]
	v_cmp_le_u32_e64 s[12:13], s6, v156
	v_addc_co_u32_e64 v8, s[20:21], 0, v8, s[16:17]
	v_cmp_le_u32_e64 s[16:17], s6, v157
	v_addc_co_u32_e64 v8, s[20:21], 0, v8, s[8:9]
	v_cmp_le_u32_e64 s[8:9], s6, v158
	v_addc_co_u32_e64 v8, s[20:21], 0, v8, s[12:13]
	v_cmp_le_u32_e64 s[12:13], s6, v159
	v_addc_co_u32_e64 v8, s[20:21], 0, v8, s[16:17]
	v_cmp_le_u32_e64 s[16:17], s6, v161
	v_addc_co_u32_e64 v8, s[20:21], 0, v8, s[8:9]
	v_cmp_le_u32_e64 s[8:9], s6, v164
	v_addc_co_u32_e64 v8, s[20:21], 0, v8, s[12:13]
	v_cmp_le_u32_e64 s[12:13], s6, v170
	v_addc_co_u32_e64 v8, s[20:21], 0, v8, s[16:17]
	v_cmp_le_u32_e64 s[16:17], s6, v171
	v_addc_co_u32_e64 v8, s[20:21], 0, v8, s[8:9]
	v_cmp_le_u32_e64 s[8:9], s6, v173
	v_addc_co_u32_e64 v8, s[20:21], 0, v8, s[12:13]
	v_cmp_le_u32_e64 s[12:13], s6, v180
	v_addc_co_u32_e64 v8, s[20:21], 0, v8, s[16:17]
	v_cmp_le_u32_e64 s[16:17], s6, v182
	v_addc_co_u32_e64 v8, s[20:21], 0, v8, s[8:9]
	v_cmp_le_u32_e64 s[8:9], s6, v184
	v_addc_co_u32_e64 v8, s[20:21], 0, v8, s[12:13]
	v_cmp_le_u32_e64 s[12:13], s6, v186
	v_addc_co_u32_e64 v8, s[20:21], 0, v8, s[16:17]
	v_cmp_le_u32_e64 s[16:17], s6, v188
	v_addc_co_u32_e64 v8, s[20:21], 0, v8, s[8:9]
	v_cmp_le_u32_e64 s[8:9], s6, v197
	v_addc_co_u32_e64 v8, s[20:21], 0, v8, s[12:13]
	v_cmp_le_u32_e64 s[12:13], s6, v199
	v_addc_co_u32_e64 v8, s[20:21], 0, v8, s[16:17]
	v_cmp_le_u32_e64 s[16:17], s6, v201
	v_addc_co_u32_e64 v8, s[20:21], 0, v8, s[8:9]
	v_cmp_le_u32_e64 s[8:9], s6, v202
	v_addc_co_u32_e64 v8, s[20:21], 0, v8, s[12:13]
	v_cmp_le_u32_e64 s[12:13], s6, v203
	v_addc_co_u32_e64 v8, s[20:21], 0, v8, s[16:17]
	v_cmp_le_u32_e64 s[16:17], s6, v204
	v_addc_co_u32_e64 v8, s[20:21], 0, v8, s[8:9]
	v_cmp_le_u32_e64 s[8:9], s6, v205
	v_addc_co_u32_e64 v8, s[20:21], 0, v8, s[12:13]
	v_cmp_le_u32_e64 s[12:13], s6, v7
	v_addc_co_u32_e64 v8, s[20:21], 0, v8, s[16:17]
	v_addc_co_u32_e64 v8, s[20:21], 0, v8, s[8:9]
	v_addc_co_u32_e64 v8, s[20:21], 0, v8, s[12:13]
	v_and_b32_e32 v9, 32, v8
	v_cmp_ne_u32_e64 s[0:1], 0, v9
	v_and_b32_e32 v9, 16, v8
	v_cmp_ne_u32_e64 s[22:23], 0, v9
	v_and_b32_e32 v9, 8, v8
	v_cmp_ne_u32_e64 s[18:19], 0, v9
	v_and_b32_e32 v9, 4, v8
	v_cmp_ne_u32_e64 s[16:17], 0, v9
	v_and_b32_e32 v9, 2, v8
	v_cmp_ne_u32_e64 s[12:13], 0, v9
	v_and_b32_e32 v9, 1, v8
	v_cmp_ne_u32_e64 s[8:9], 0, v9
	s_bcnt1_i32_b64 s7, s[0:1]
	s_bcnt1_i32_b64 s3, s[22:23]
	s_lshl1_add_u32 s7, s7, s3
	s_bcnt1_i32_b64 s3, s[18:19]
	s_lshl1_add_u32 s7, s7, s3
	s_bcnt1_i32_b64 s3, s[16:17]
	s_lshl1_add_u32 s7, s7, s3
	s_bcnt1_i32_b64 s3, s[12:13]
	s_lshl1_add_u32 s7, s7, s3
	s_bcnt1_i32_b64 s3, s[8:9]
	s_lshl1_add_u32 s7, s7, s3
	s_cmpk_lt_u32 s7, 0x100
	s_cselect_b32 s4, s4, s6
	s_cmpk_eq_u32 s7, 0x100
	s_cbranch_scc1 .Ltk1_x32
	s_lshr_b32 s5, s5, 1
	s_cbranch_scc1 .Ltk1_l32
	s_branch .Ltk1_orig
.Ltk1_l24:
	s_or_b32 s6, s4, s5
	v_cmp_le_u32_e64 s[8:9], s6, v140
	v_cmp_le_u32_e64 s[12:13], s6, v142
	v_cmp_le_u32_e64 s[16:17], s6, v144
	v_cndmask_b32_e64 v8, 0, 1, s[8:9]
	v_cmp_le_u32_e64 s[8:9], s6, v146
	v_addc_co_u32_e64 v8, s[20:21], 0, v8, s[12:13]
	v_cmp_le_u32_e64 s[12:13], s6, v148
	v_addc_co_u32_e64 v8, s[20:21], 0, v8, s[16:17]
	v_cmp_le_u32_e64 s[16:17], s6, v150
	v_addc_co_u32_e64 v8, s[20:21], 0, v8, s[8:9]
	v_cmp_le_u32_e64 s[8:9], s6, v152
	v_addc_co_u32_e64 v8, s[20:21], 0, v8, s[12:13]
	v_cmp_le_u32_e64 s[12:13], s6, v153
	v_addc_co_u32_e64 v8, s[20:21], 0, v8, s[16:17]
	v_cmp_le_u32_e64 s[16:17], s6, v154
	v_addc_co_u32_e64 v8, s[20:21], 0, v8, s[8:9]
	v_cmp_le_u32_e64 s[8:9], s6, v155
	v_addc_co_u32_e64 v8, s[20:21], 0, v8, s[12:13]
	v_cmp_le_u32_e64 s[12:13], s6, v156
	v_addc_co_u32_e64 v8, s[20:21], 0, v8, s[16:17]
	v_cmp_le_u32_e64 s[16:17], s6, v157
	v_addc_co_u32_e64 v8, s[20:21], 0, v8, s[8:9]
	v_cmp_le_u32_e64 s[8:9], s6, v158
	v_addc_co_u32_e64 v8, s[20:21], 0, v8, s[12:13]
	v_cmp_le_u32_e64 s[12:13], s6, v159
	v_addc_co_u32_e64 v8, s[20:21], 0, v8, s[16:17]
	v_cmp_le_u32_e64 s[16:17], s6, v161
	v_addc_co_u32_e64 v8, s[20:21], 0, v8, s[8:9]
	v_cmp_le_u32_e64 s[8:9], s6, v164
	v_addc_co_u32_e64 v8, s[20:21], 0, v8, s[12:13]
	v_cmp_le_u32_e64 s[12:13], s6, v170
	v_addc_co_u32_e64 v8, s[20:21], 0, v8, s[16:17]
	v_cmp_le_u32_e64 s[16:17], s6, v171
	v_addc_co_u32_e64 v8, s[20:21], 0, v8, s[8:9]
	v_cmp_le_u32_e64 s[8:9], s6, v173
	v_addc_co_u32_e64 v8, s[20:21], 0, v8, s[12:13]
	v_cmp_le_u32_e64 s[12:13], s6, v180
	v_addc_co_u32_e64 v8, s[20:21], 0, v8, s[16:17]
	v_cmp_le_u32_e64 s[16:17], s6, v182
	v_addc_co_u32_e64 v8, s[20:21], 0, v8, s[8:9]
	v_cmp_le_u32_e64 s[8:9], s6, v184
	v_addc_co_u32_e64 v8, s[20:21], 0, v8, s[12:13]
	v_cmp_le_u32_e64 s[12:13], s6, v186
	v_addc_co_u32_e64 v8, s[20:21], 0, v8, s[16:17]
	v_cmp_le_u32_e64 s[16:17], s6, v188
	v_addc_co_u32_e64 v8, s[20:21], 0, v8, s[8:9]
	v_addc_co_u32_e64 v8, s[20:21], 0, v8, s[12:13]
	v_addc_co_u32_e64 v8, s[20:21], 0, v8, s[16:17]
	v_and_b32_e32 v9, 16, v8
	v_cmp_ne_u32_e64 s[22:23], 0, v9
	v_and_b32_e32 v9, 8, v8
	v_cmp_ne_u32_e64 s[18:19], 0, v9
	v_and_b32_e32 v9, 4, v8
	v_cmp_ne_u32_e64 s[16:17], 0, v9
	v_and_b32_e32 v9, 2, v8
	v_cmp_ne_u32_e64 s[12:13], 0, v9
	v_and_b32_e32 v9, 1, v8
	v_cmp_ne_u32_e64 s[8:9], 0, v9
	s_bcnt1_i32_b64 s7, s[22:23]
	s_bcnt1_i32_b64 s3, s[18:19]
	s_lshl1_add_u32 s7, s7, s3
	s_bcnt1_i32_b64 s3, s[16:17]
	s_lshl1_add_u32 s7, s7, s3
	s_bcnt1_i32_b64 s3, s[12:13]
	s_lshl1_add_u32 s7, s7, s3
	s_bcnt1_i32_b64 s3, s[8:9]
	s_lshl1_add_u32 s7, s7, s3
	s_cmpk_lt_u32 s7, 0x100
	s_cselect_b32 s4, s4, s6
	s_cmpk_eq_u32 s7, 0x100
	s_cbranch_scc1 .Ltk1_x24
	s_lshr_b32 s5, s5, 1
	s_cbranch_scc1 .Ltk1_l24
	s_branch .Ltk1_orig
.Ltk1_l16:
	s_or_b32 s6, s4, s5
	v_cmp_le_u32_e64 s[8:9], s6, v140
	v_cmp_le_u32_e64 s[12:13], s6, v142
	v_cmp_le_u32_e64 s[16:17], s6, v144
	v_cndmask_b32_e64 v8, 0, 1, s[8:9]
	v_cmp_le_u32_e64 s[8:9], s6, v146
	v_addc_co_u32_e64 v8, s[20:21], 0, v8, s[12:13]
	v_cmp_le_u32_e64 s[12:13], s6, v148
	v_addc_co_u32_e64 v8, s[20:21], 0, v8, s[16:17]
	v_cmp_le_u32_e64 s[16:17], s6, v150
	v_addc_co_u32_e64 v8, s[20:21], 0, v8, s[8:9]
	v_cmp_le_u32_e64 s[8:9], s6, v152
	v_addc_co_u32_e64 v8, s[20:21], 0, v8, s[12:13]
	v_cmp_le_u32_e64 s[12:13], s6, v153
	v_addc_co_u32_e64 v8, s[20:21], 0, v8, s[16:17]
	v_cmp_le_u32_e64 s[16:17], s6, v154
	v_addc_co_u32_e64 v8, s[20:21], 0, v8, s[8:9]
	v_cmp_le_u32_e64 s[8:9], s6, v155
	v_addc_co_u32_e64 v8, s[20:21], 0, v8, s[12:13]
	v_cmp_le_u32_e64 s[12:13], s6, v156
	v_addc_co_u32_e64 v8, s[20:21], 0, v8, s[16:17]
	v_cmp_le_u32_e64 s[16:17], s6, v157
	v_addc_co_u32_e64 v8, s[20:21], 0, v8, s[8:9]
	v_cmp_le_u32_e64 s[8:9], s6, v158
	v_addc_co_u32_e64 v8, s[20:21], 0, v8, s[12:13]
	v_cmp_le_u32_e64 s[12:13], s6, v159
	v_addc_co_u32_e64 v8, s[20:21], 0, v8, s[16:17]
	v_cmp_le_u32_e64 s[16:17], s6, v161
	v_addc_co_u32_e64 v8, s[20:21], 0, v8, s[8:9]
	v_cmp_le_u32_e64 s[8:9], s6, v164
	v_addc_co_u32_e64 v8, s[20:21], 0, v8, s[12:13]
	v_addc_co_u32_e64 v8, s[20:21], 0, v8, s[16:17]
	v_addc_co_u32_e64 v8, s[20:21], 0, v8, s[8:9]
	v_and_b32_e32 v9, 16, v8
	v_cmp_ne_u32_e64 s[22:23], 0, v9
	v_and_b32_e32 v9, 8, v8
	v_cmp_ne_u32_e64 s[18:19], 0, v9
	v_and_b32_e32 v9, 4, v8
	v_cmp_ne_u32_e64 s[16:17], 0, v9
	v_and_b32_e32 v9, 2, v8
	v_cmp_ne_u32_e64 s[12:13], 0, v9
	v_and_b32_e32 v9, 1, v8
	v_cmp_ne_u32_e64 s[8:9], 0, v9
	s_bcnt1_i32_b64 s7, s[22:23]
	s_bcnt1_i32_b64 s3, s[18:19]
	s_lshl1_add_u32 s7, s7, s3
	s_bcnt1_i32_b64 s3, s[16:17]
	s_lshl1_add_u32 s7, s7, s3
	s_bcnt1_i32_b64 s3, s[12:13]
	s_lshl1_add_u32 s7, s7, s3
	s_bcnt1_i32_b64 s3, s[8:9]
	s_lshl1_add_u32 s7, s7, s3
	s_cmpk_lt_u32 s7, 0x100
	s_cselect_b32 s4, s4, s6
	s_cmpk_eq_u32 s7, 0x100
	s_cbranch_scc1 .Ltk1_x16
	s_lshr_b32 s5, s5, 1
	s_cbranch_scc1 .Ltk1_l16
	s_branch .Ltk1_orig
.Ltk1_l8:
	s_or_b32 s6, s4, s5
	v_cmp_le_u32_e64 s[8:9], s6, v140
	v_cmp_le_u32_e64 s[12:13], s6, v142
	v_cmp_le_u32_e64 s[16:17], s6, v144
	v_cndmask_b32_e64 v8, 0, 1, s[8:9]
	v_cmp_le_u32_e64 s[8:9], s6, v146
	v_addc_co_u32_e64 v8, s[20:21], 0, v8, s[12:13]
	v_cmp_le_u32_e64 s[12:13], s6, v148
	v_addc_co_u32_e64 v8, s[20:21], 0, v8, s[16:17]
	v_cmp_le_u32_e64 s[16:17], s6, v150
	v_addc_co_u32_e64 v8, s[20:21], 0, v8, s[8:9]
	v_cmp_le_u32_e64 s[8:9], s6, v152
	v_addc_co_u32_e64 v8, s[20:21], 0, v8, s[12:13]
	v_cmp_le_u32_e64 s[12:13], s6, v153
	v_addc_co_u32_e64 v8, s[20:21], 0, v8, s[16:17]
	v_addc_co_u32_e64 v8, s[20:21], 0, v8, s[8:9]
	v_addc_co_u32_e64 v8, s[20:21], 0, v8, s[12:13]
	v_and_b32_e32 v9, 8, v8
	v_cmp_ne_u32_e64 s[18:19], 0, v9
	v_and_b32_e32 v9, 4, v8
	v_cmp_ne_u32_e64 s[16:17], 0, v9
	v_and_b32_e32 v9, 2, v8
	v_cmp_ne_u32_e64 s[12:13], 0, v9
	v_and_b32_e32 v9, 1, v8
	v_cmp_ne_u32_e64 s[8:9], 0, v9
	s_bcnt1_i32_b64 s7, s[18:19]
	s_bcnt1_i32_b64 s3, s[16:17]
	s_lshl1_add_u32 s7, s7, s3
	s_bcnt1_i32_b64 s3, s[12:13]
	s_lshl1_add_u32 s7, s7, s3
	s_bcnt1_i32_b64 s3, s[8:9]
	s_lshl1_add_u32 s7, s7, s3
	s_cmpk_lt_u32 s7, 0x100
	s_cselect_b32 s4, s4, s6
	s_cmpk_eq_u32 s7, 0x100
	s_cbranch_scc1 .Ltk1_x8
	s_lshr_b32 s5, s5, 1
	s_cbranch_scc1 .Ltk1_l8
	s_branch .Ltk1_orig
.Ltk1_x32:
	v_cmp_le_u32_e64 s[8:9], s4, v140
	v_cmp_le_u32_e64 s[12:13], s4, v142
	v_cmp_le_u32_e64 s[16:17], s4, v144
	s_nop 0
	v_writelane_b32 v10, s8, 0
	v_writelane_b32 v11, s9, 0
	v_cmp_le_u32_e64 s[8:9], s4, v146
	v_writelane_b32 v10, s12, 1
	v_writelane_b32 v11, s13, 1
	v_cmp_le_u32_e64 s[12:13], s4, v148
	v_writelane_b32 v10, s16, 2
	v_writelane_b32 v11, s17, 2
	v_cmp_le_u32_e64 s[16:17], s4, v150
	v_writelane_b32 v10, s8, 3
	v_writelane_b32 v11, s9, 3
	v_cmp_le_u32_e64 s[8:9], s4, v152
	v_writelane_b32 v10, s12, 4
	v_writelane_b32 v11, s13, 4
	v_cmp_le_u32_e64 s[12:13], s4, v153
	v_writelane_b32 v10, s16, 5
	v_writelane_b32 v11, s17, 5
	v_cmp_le_u32_e64 s[16:17], s4, v154
	v_writelane_b32 v10, s8, 6
	v_writelane_b32 v11, s9, 6
	v_cmp_le_u32_e64 s[8:9], s4, v155
	v_writelane_b32 v10, s12, 7
	v_writelane_b32 v11, s13, 7
	v_cmp_le_u32_e64 s[12:13], s4, v156
	v_writelane_b32 v10, s16, 8
	v_writelane_b32 v11, s17, 8
	v_cmp_le_u32_e64 s[16:17], s4, v157
	v_writelane_b32 v10, s8, 9
	v_writelane_b32 v11, s9, 9
	v_cmp_le_u32_e64 s[8:9], s4, v158
	v_writelane_b32 v10, s12, 10
	v_writelane_b32 v11, s13, 10
	v_cmp_le_u32_e64 s[12:13], s4, v159
	v_writelane_b32 v10, s16, 11
	v_writelane_b32 v11, s17, 11
	v_cmp_le_u32_e64 s[16:17], s4, v161
	v_writelane_b32 v10, s8, 12
	v_writelane_b32 v11, s9, 12
	v_cmp_le_u32_e64 s[8:9], s4, v164
	v_writelane_b32 v10, s12, 13
	v_writelane_b32 v11, s13, 13
	v_cmp_le_u32_e64 s[12:13], s4, v170
	v_writelane_b32 v10, s16, 14
	v_writelane_b32 v11, s17, 14
	v_cmp_le_u32_e64 s[16:17], s4, v171
	v_writelane_b32 v10, s8, 15
	v_writelane_b32 v11, s9, 15
	v_cmp_le_u32_e64 s[8:9], s4, v173
	v_writelane_b32 v10, s12, 16
	v_writelane_b32 v11, s13, 16
	v_cmp_le_u32_e64 s[12:13], s4, v180
	v_writelane_b32 v10, s16, 17
	v_writelane_b32 v11, s17, 17
	v_cmp_le_u32_e64 s[16:17], s4, v182
	v_writelane_b32 v10, s8, 18
	v_writelane_b32 v11, s9, 18
	v_cmp_le_u32_e64 s[8:9], s4, v184
	v_writelane_b32 v10, s12, 19
	v_writelane_b32 v11, s13, 19
	v_cmp_le_u32_e64 s[12:13], s4, v186
	v_writelane_b32 v10, s16, 20
	v_writelane_b32 v11, s17, 20
	v_cmp_le_u32_e64 s[16:17], s4, v188
	v_writelane_b32 v10, s8, 21
	v_writelane_b32 v11, s9, 21
	v_cmp_le_u32_e64 s[8:9], s4, v197
	v_writelane_b32 v10, s12, 22
	v_writelane_b32 v11, s13, 22
	v_cmp_le_u32_e64 s[12:13], s4, v199
	v_writelane_b32 v10, s16, 23
	v_writelane_b32 v11, s17, 23
	v_cmp_le_u32_e64 s[16:17], s4, v201
	v_writelane_b32 v10, s8, 24
	v_writelane_b32 v11, s9, 24
	v_cmp_le_u32_e64 s[8:9], s4, v202
	v_writelane_b32 v10, s12, 25
	v_writelane_b32 v11, s13, 25
	v_cmp_le_u32_e64 s[12:13], s4, v203
	v_writelane_b32 v10, s16, 26
	v_writelane_b32 v11, s17, 26
	v_cmp_le_u32_e64 s[16:17], s4, v204
	v_writelane_b32 v10, s8, 27
	v_writelane_b32 v11, s9, 27
	v_cmp_le_u32_e64 s[8:9], s4, v205
	v_writelane_b32 v10, s12, 28
	v_writelane_b32 v11, s13, 28
	v_cmp_le_u32_e64 s[12:13], s4, v7
	v_writelane_b32 v10, s16, 29
	v_writelane_b32 v11, s17, 29
	v_writelane_b32 v10, s8, 30
	v_writelane_b32 v11, s9, 30
	v_writelane_b32 v10, s12, 31
	v_writelane_b32 v11, s13, 31
	v_mov_b32_e32 v2, v10
	v_mov_b32_e32 v3, v11
	s_branch .LBB0_2149
.Ltk1_x24:
	v_cmp_le_u32_e64 s[8:9], s4, v140
	v_cmp_le_u32_e64 s[12:13], s4, v142
	v_cmp_le_u32_e64 s[16:17], s4, v144
	s_nop 0
	v_writelane_b32 v10, s8, 0
	v_writelane_b32 v11, s9, 0
	v_cmp_le_u32_e64 s[8:9], s4, v146
	v_writelane_b32 v10, s12, 1
	v_writelane_b32 v11, s13, 1
	v_cmp_le_u32_e64 s[12:13], s4, v148
	v_writelane_b32 v10, s16, 2
	v_writelane_b32 v11, s17, 2
	v_cmp_le_u32_e64 s[16:17], s4, v150
	v_writelane_b32 v10, s8, 3
	v_writelane_b32 v11, s9, 3
	v_cmp_le_u32_e64 s[8:9], s4, v152
	v_writelane_b32 v10, s12, 4
	v_writelane_b32 v11, s13, 4
	v_cmp_le_u32_e64 s[12:13], s4, v153
	v_writelane_b32 v10, s16, 5
	v_writelane_b32 v11, s17, 5
	v_cmp_le_u32_e64 s[16:17], s4, v154
	v_writelane_b32 v10, s8, 6
	v_writelane_b32 v11, s9, 6
	v_cmp_le_u32_e64 s[8:9], s4, v155
	v_writelane_b32 v10, s12, 7
	v_writelane_b32 v11, s13, 7
	v_cmp_le_u32_e64 s[12:13], s4, v156
	v_writelane_b32 v10, s16, 8
	v_writelane_b32 v11, s17, 8
	v_cmp_le_u32_e64 s[16:17], s4, v157
	v_writelane_b32 v10, s8, 9
	v_writelane_b32 v11, s9, 9
	v_cmp_le_u32_e64 s[8:9], s4, v158
	v_writelane_b32 v10, s12, 10
	v_writelane_b32 v11, s13, 10
	v_cmp_le_u32_e64 s[12:13], s4, v159
	v_writelane_b32 v10, s16, 11
	v_writelane_b32 v11, s17, 11
	v_cmp_le_u32_e64 s[16:17], s4, v161
	v_writelane_b32 v10, s8, 12
	v_writelane_b32 v11, s9, 12
	v_cmp_le_u32_e64 s[8:9], s4, v164
	v_writelane_b32 v10, s12, 13
	v_writelane_b32 v11, s13, 13
	v_cmp_le_u32_e64 s[12:13], s4, v170
	v_writelane_b32 v10, s16, 14
	v_writelane_b32 v11, s17, 14
	v_cmp_le_u32_e64 s[16:17], s4, v171
	v_writelane_b32 v10, s8, 15
	v_writelane_b32 v11, s9, 15
	v_cmp_le_u32_e64 s[8:9], s4, v173
	v_writelane_b32 v10, s12, 16
	v_writelane_b32 v11, s13, 16
	v_cmp_le_u32_e64 s[12:13], s4, v180
	v_writelane_b32 v10, s16, 17
	v_writelane_b32 v11, s17, 17
	v_cmp_le_u32_e64 s[16:17], s4, v182
	v_writelane_b32 v10, s8, 18
	v_writelane_b32 v11, s9, 18
	v_cmp_le_u32_e64 s[8:9], s4, v184
	v_writelane_b32 v10, s12, 19
	v_writelane_b32 v11, s13, 19
	v_cmp_le_u32_e64 s[12:13], s4, v186
	v_writelane_b32 v10, s16, 20
	v_writelane_b32 v11, s17, 20
	v_cmp_le_u32_e64 s[16:17], s4, v188
	v_writelane_b32 v10, s8, 21
	v_writelane_b32 v11, s9, 21
	v_writelane_b32 v10, s12, 22
	v_writelane_b32 v11, s13, 22
	v_writelane_b32 v10, s16, 23
	v_writelane_b32 v11, s17, 23
	v_mov_b32_e32 v2, v10
	v_mov_b32_e32 v3, v11
	s_branch .LBB0_2149
.Ltk1_x16:
	v_cmp_le_u32_e64 s[8:9], s4, v140
	v_cmp_le_u32_e64 s[12:13], s4, v142
	v_cmp_le_u32_e64 s[16:17], s4, v144
	s_nop 0
	v_writelane_b32 v10, s8, 0
	v_writelane_b32 v11, s9, 0
	v_cmp_le_u32_e64 s[8:9], s4, v146
	v_writelane_b32 v10, s12, 1
	v_writelane_b32 v11, s13, 1
	v_cmp_le_u32_e64 s[12:13], s4, v148
	v_writelane_b32 v10, s16, 2
	v_writelane_b32 v11, s17, 2
	v_cmp_le_u32_e64 s[16:17], s4, v150
	v_writelane_b32 v10, s8, 3
	v_writelane_b32 v11, s9, 3
	v_cmp_le_u32_e64 s[8:9], s4, v152
	v_writelane_b32 v10, s12, 4
	v_writelane_b32 v11, s13, 4
	v_cmp_le_u32_e64 s[12:13], s4, v153
	v_writelane_b32 v10, s16, 5
	v_writelane_b32 v11, s17, 5
	v_cmp_le_u32_e64 s[16:17], s4, v154
	v_writelane_b32 v10, s8, 6
	v_writelane_b32 v11, s9, 6
	v_cmp_le_u32_e64 s[8:9], s4, v155
	v_writelane_b32 v10, s12, 7
	v_writelane_b32 v11, s13, 7
	v_cmp_le_u32_e64 s[12:13], s4, v156
	v_writelane_b32 v10, s16, 8
	v_writelane_b32 v11, s17, 8
	v_cmp_le_u32_e64 s[16:17], s4, v157
	v_writelane_b32 v10, s8, 9
	v_writelane_b32 v11, s9, 9
	v_cmp_le_u32_e64 s[8:9], s4, v158
	v_writelane_b32 v10, s12, 10
	v_writelane_b32 v11, s13, 10
	v_cmp_le_u32_e64 s[12:13], s4, v159
	v_writelane_b32 v10, s16, 11
	v_writelane_b32 v11, s17, 11
	v_cmp_le_u32_e64 s[16:17], s4, v161
	v_writelane_b32 v10, s8, 12
	v_writelane_b32 v11, s9, 12
	v_cmp_le_u32_e64 s[8:9], s4, v164
	v_writelane_b32 v10, s12, 13
	v_writelane_b32 v11, s13, 13
	v_writelane_b32 v10, s16, 14
	v_writelane_b32 v11, s17, 14
	v_writelane_b32 v10, s8, 15
	v_writelane_b32 v11, s9, 15
	v_mov_b32_e32 v2, v10
	v_mov_b32_e32 v3, v11
	s_branch .LBB0_2149
.Ltk1_x8:
	v_cmp_le_u32_e64 s[8:9], s4, v140
	v_cmp_le_u32_e64 s[12:13], s4, v142
	v_cmp_le_u32_e64 s[16:17], s4, v144
	s_nop 0
	v_writelane_b32 v10, s8, 0
	v_writelane_b32 v11, s9, 0
	v_cmp_le_u32_e64 s[8:9], s4, v146
	v_writelane_b32 v10, s12, 1
	v_writelane_b32 v11, s13, 1
	v_cmp_le_u32_e64 s[12:13], s4, v148
	v_writelane_b32 v10, s16, 2
	v_writelane_b32 v11, s17, 2
	v_cmp_le_u32_e64 s[16:17], s4, v150
	v_writelane_b32 v10, s8, 3
	v_writelane_b32 v11, s9, 3
	v_cmp_le_u32_e64 s[8:9], s4, v152
	v_writelane_b32 v10, s12, 4
	v_writelane_b32 v11, s13, 4
	v_cmp_le_u32_e64 s[12:13], s4, v153
	v_writelane_b32 v10, s16, 5
	v_writelane_b32 v11, s17, 5
	v_writelane_b32 v10, s8, 6
	v_writelane_b32 v11, s9, 6
	v_writelane_b32 v10, s12, 7
	v_writelane_b32 v11, s13, 7
	v_mov_b32_e32 v2, v10
	v_mov_b32_e32 v3, v11
	s_branch .LBB0_2149
.Ltk1_orig:
	s_and_b64 vcc, exec, s[26:27]
	s_cbranch_vccz .LBB0_1990
	v_readlane_b32 s0, v252, 55
	v_readlane_b32 s1, v252, 56
	s_and_b64 vcc, exec, s[0:1]
	s_cbranch_vccz .LBB0_1991
	v_readlane_b32 s0, v254, 37
	v_readlane_b32 s1, v254, 38
	s_and_b64 vcc, exec, s[0:1]
	s_cbranch_vccz .LBB0_1992
	v_mov_b32_e32 v3, 31
	v_mov_b32_e32 v2, 0

.Ltk2_l32:
	s_or_b32 s6, s4, s5
	v_cmp_le_u32_e64 s[8:9], s6, v111
	v_cmp_le_u32_e64 s[12:13], s6, v113
	v_cmp_le_u32_e64 s[16:17], s6, v115
	v_cndmask_b32_e64 v8, 0, 1, s[8:9]
	v_cmp_le_u32_e64 s[8:9], s6, v117
	v_addc_co_u32_e64 v8, s[20:21], 0, v8, s[12:13]
	v_cmp_le_u32_e64 s[12:13], s6, v119
	v_addc_co_u32_e64 v8, s[20:21], 0, v8, s[16:17]
	v_cmp_le_u32_e64 s[16:17], s6, v121
	v_addc_co_u32_e64 v8, s[20:21], 0, v8, s[8:9]
	v_cmp_le_u32_e64 s[8:9], s6, v123
	v_addc_co_u32_e64 v8, s[20:21], 0, v8, s[12:13]
	v_cmp_le_u32_e64 s[12:13], s6, v124
	v_addc_co_u32_e64 v8, s[20:21], 0, v8, s[16:17]
	v_cmp_le_u32_e64 s[16:17], s6, v125
	v_addc_co_u32_e64 v8, s[20:21], 0, v8, s[8:9]
	v_cmp_le_u32_e64 s[8:9], s6, v126
	v_addc_co_u32_e64 v8, s[20:21], 0, v8, s[12:13]
	v_cmp_le_u32_e64 s[12:13], s6, v127
	v_addc_co_u32_e64 v8, s[20:21], 0, v8, s[16:17]
	v_cmp_le_u32_e64 s[16:17], s6, v128
	v_addc_co_u32_e64 v8, s[20:21], 0, v8, s[8:9]
	v_cmp_le_u32_e64 s[8:9], s6, v129
	v_addc_co_u32_e64 v8, s[20:21], 0, v8, s[12:13]
	v_cmp_le_u32_e64 s[12:13], s6, v130
	v_addc_co_u32_e64 v8, s[20:21], 0, v8, s[16:17]
	v_cmp_le_u32_e64 s[16:17], s6, v132
	v_addc_co_u32_e64 v8, s[20:21], 0, v8, s[8:9]
	v_cmp_le_u32_e64 s[8:9], s6, v133
	v_addc_co_u32_e64 v8, s[20:21], 0, v8, s[12:13]
	v_cmp_le_u32_e64 s[12:13], s6, v138
	v_addc_co_u32_e64 v8, s[20:21], 0, v8, s[16:17]
	v_cmp_le_u32_e64 s[16:17], s6, v139
	v_addc_co_u32_e64 v8, s[20:21], 0, v8, s[8:9]
	v_cmp_le_u32_e64 s[8:9], s6, v141
	v_addc_co_u32_e64 v8, s[20:21], 0, v8, s[12:13]
	v_cmp_le_u32_e64 s[12:13], s6, v143
	v_addc_co_u32_e64 v8, s[20:21], 0, v8, s[16:17]
	v_cmp_le_u32_e64 s[16:17], s6, v145
	v_addc_co_u32_e64 v8, s[20:21], 0, v8, s[8:9]
	v_cmp_le_u32_e64 s[8:9], s6, v147
	v_addc_co_u32_e64 v8, s[20:21], 0, v8, s[12:13]
	v_cmp_le_u32_e64 s[12:13], s6, v149
	v_addc_co_u32_e64 v8, s[20:21], 0, v8, s[16:17]
	v_cmp_le_u32_e64 s[16:17], s6, v151
	v_addc_co_u32_e64 v8, s[20:21], 0, v8, s[8:9]
	v_cmp_le_u32_e64 s[8:9], s6, v160
	v_addc_co_u32_e64 v8, s[20:21], 0, v8, s[12:13]
	v_cmp_le_u32_e64 s[12:13], s6, v163
	v_addc_co_u32_e64 v8, s[20:21], 0, v8, s[16:17]
	v_cmp_le_u32_e64 s[16:17], s6, v165
	v_addc_co_u32_e64 v8, s[20:21], 0, v8, s[8:9]
	v_cmp_le_u32_e64 s[8:9], s6, v166
	v_addc_co_u32_e64 v8, s[20:21], 0, v8, s[12:13]
	v_cmp_le_u32_e64 s[12:13], s6, v167
	v_addc_co_u32_e64 v8, s[20:21], 0, v8, s[16:17]
	v_cmp_le_u32_e64 s[16:17], s6, v168
	v_addc_co_u32_e64 v8, s[20:21], 0, v8, s[8:9]
	v_cmp_le_u32_e64 s[8:9], s6, v169
	v_addc_co_u32_e64 v8, s[20:21], 0, v8, s[12:13]
	v_cmp_le_u32_e64 s[12:13], s6, v6
	v_addc_co_u32_e64 v8, s[20:21], 0, v8, s[16:17]
	v_addc_co_u32_e64 v8, s[20:21], 0, v8, s[8:9]
	v_addc_co_u32_e64 v8, s[20:21], 0, v8, s[12:13]
	v_and_b32_e32 v9, 32, v8
	v_cmp_ne_u32_e64 s[0:1], 0, v9
	v_and_b32_e32 v9, 16, v8
	v_cmp_ne_u32_e64 s[22:23], 0, v9
	v_and_b32_e32 v9, 8, v8
	v_cmp_ne_u32_e64 s[18:19], 0, v9
	v_and_b32_e32 v9, 4, v8
	v_cmp_ne_u32_e64 s[16:17], 0, v9
	v_and_b32_e32 v9, 2, v8
	v_cmp_ne_u32_e64 s[12:13], 0, v9
	v_and_b32_e32 v9, 1, v8
	v_cmp_ne_u32_e64 s[8:9], 0, v9
	s_bcnt1_i32_b64 s7, s[0:1]
	s_bcnt1_i32_b64 s3, s[22:23]
	s_lshl1_add_u32 s7, s7, s3
	s_bcnt1_i32_b64 s3, s[18:19]
	s_lshl1_add_u32 s7, s7, s3
	s_bcnt1_i32_b64 s3, s[16:17]
	s_lshl1_add_u32 s7, s7, s3
	s_bcnt1_i32_b64 s3, s[12:13]
	s_lshl1_add_u32 s7, s7, s3
	s_bcnt1_i32_b64 s3, s[8:9]
	s_lshl1_add_u32 s7, s7, s3
	s_cmpk_lt_u32 s7, 0x100
	s_cselect_b32 s4, s4, s6
	s_cmpk_eq_u32 s7, 0x100
	s_cbranch_scc1 .Ltk2_x32
	s_lshr_b32 s5, s5, 1
	s_cbranch_scc1 .Ltk2_l32
	s_branch .Ltk2_orig
.Ltk2_l24:
	s_or_b32 s6, s4, s5
	v_cmp_le_u32_e64 s[8:9], s6, v111
	v_cmp_le_u32_e64 s[12:13], s6, v113
	v_cmp_le_u32_e64 s[16:17], s6, v115
	v_cndmask_b32_e64 v8, 0, 1, s[8:9]
	v_cmp_le_u32_e64 s[8:9], s6, v117
	v_addc_co_u32_e64 v8, s[20:21], 0, v8, s[12:13]
	v_cmp_le_u32_e64 s[12:13], s6, v119
	v_addc_co_u32_e64 v8, s[20:21], 0, v8, s[16:17]
	v_cmp_le_u32_e64 s[16:17], s6, v121
	v_addc_co_u32_e64 v8, s[20:21], 0, v8, s[8:9]
	v_cmp_le_u32_e64 s[8:9], s6, v123
	v_addc_co_u32_e64 v8, s[20:21], 0, v8, s[12:13]
	v_cmp_le_u32_e64 s[12:13], s6, v124
	v_addc_co_u32_e64 v8, s[20:21], 0, v8, s[16:17]
	v_cmp_le_u32_e64 s[16:17], s6, v125
	v_addc_co_u32_e64 v8, s[20:21], 0, v8, s[8:9]
	v_cmp_le_u32_e64 s[8:9], s6, v126
	v_addc_co_u32_e64 v8, s[20:21], 0, v8, s[12:13]
	v_cmp_le_u32_e64 s[12:13], s6, v127
	v_addc_co_u32_e64 v8, s[20:21], 0, v8, s[16:17]
	v_cmp_le_u32_e64 s[16:17], s6, v128
	v_addc_co_u32_e64 v8, s[20:21], 0, v8, s[8:9]
	v_cmp_le_u32_e64 s[8:9], s6, v129
	v_addc_co_u32_e64 v8, s[20:21], 0, v8, s[12:13]
	v_cmp_le_u32_e64 s[12:13], s6, v130
	v_addc_co_u32_e64 v8, s[20:21], 0, v8, s[16:17]
	v_cmp_le_u32_e64 s[16:17], s6, v132
	v_addc_co_u32_e64 v8, s[20:21], 0, v8, s[8:9]
	v_cmp_le_u32_e64 s[8:9], s6, v133
	v_addc_co_u32_e64 v8, s[20:21], 0, v8, s[12:13]
	v_cmp_le_u32_e64 s[12:13], s6, v138
	v_addc_co_u32_e64 v8, s[20:21], 0, v8, s[16:17]
	v_cmp_le_u32_e64 s[16:17], s6, v139
	v_addc_co_u32_e64 v8, s[20:21], 0, v8, s[8:9]
	v_cmp_le_u32_e64 s[8:9], s6, v141
	v_addc_co_u32_e64 v8, s[20:21], 0, v8, s[12:13]
	v_cmp_le_u32_e64 s[12:13], s6, v143
	v_addc_co_u32_e64 v8, s[20:21], 0, v8, s[16:17]
	v_cmp_le_u32_e64 s[16:17], s6, v145
	v_addc_co_u32_e64 v8, s[20:21], 0, v8, s[8:9]
	v_cmp_le_u32_e64 s[8:9], s6, v147
	v_addc_co_u32_e64 v8, s[20:21], 0, v8, s[12:13]
	v_cmp_le_u32_e64 s[12:13], s6, v149
	v_addc_co_u32_e64 v8, s[20:21], 0, v8, s[16:17]
	v_cmp_le_u32_e64 s[16:17], s6, v151
	v_addc_co_u32_e64 v8, s[20:21], 0, v8, s[8:9]
	v_addc_co_u32_e64 v8, s[20:21], 0, v8, s[12:13]
	v_addc_co_u32_e64 v8, s[20:21], 0, v8, s[16:17]
	v_and_b32_e32 v9, 16, v8
	v_cmp_ne_u32_e64 s[22:23], 0, v9
	v_and_b32_e32 v9, 8, v8
	v_cmp_ne_u32_e64 s[18:19], 0, v9
	v_and_b32_e32 v9, 4, v8
	v_cmp_ne_u32_e64 s[16:17], 0, v9
	v_and_b32_e32 v9, 2, v8
	v_cmp_ne_u32_e64 s[12:13], 0, v9
	v_and_b32_e32 v9, 1, v8
	v_cmp_ne_u32_e64 s[8:9], 0, v9
	s_bcnt1_i32_b64 s7, s[22:23]
	s_bcnt1_i32_b64 s3, s[18:19]
	s_lshl1_add_u32 s7, s7, s3
	s_bcnt1_i32_b64 s3, s[16:17]
	s_lshl1_add_u32 s7, s7, s3
	s_bcnt1_i32_b64 s3, s[12:13]
	s_lshl1_add_u32 s7, s7, s3
	s_bcnt1_i32_b64 s3, s[8:9]
	s_lshl1_add_u32 s7, s7, s3
	s_cmpk_lt_u32 s7, 0x100
	s_cselect_b32 s4, s4, s6
	s_cmpk_eq_u32 s7, 0x100
	s_cbranch_scc1 .Ltk2_x24
	s_lshr_b32 s5, s5, 1
	s_cbranch_scc1 .Ltk2_l24
	s_branch .Ltk2_orig
.Ltk2_l16:
	s_or_b32 s6, s4, s5
	v_cmp_le_u32_e64 s[8:9], s6, v111
	v_cmp_le_u32_e64 s[12:13], s6, v113
	v_cmp_le_u32_e64 s[16:17], s6, v115
	v_cndmask_b32_e64 v8, 0, 1, s[8:9]
	v_cmp_le_u32_e64 s[8:9], s6, v117
	v_addc_co_u32_e64 v8, s[20:21], 0, v8, s[12:13]
	v_cmp_le_u32_e64 s[12:13], s6, v119
	v_addc_co_u32_e64 v8, s[20:21], 0, v8, s[16:17]
	v_cmp_le_u32_e64 s[16:17], s6, v121
	v_addc_co_u32_e64 v8, s[20:21], 0, v8, s[8:9]
	v_cmp_le_u32_e64 s[8:9], s6, v123
	v_addc_co_u32_e64 v8, s[20:21], 0, v8, s[12:13]
	v_cmp_le_u32_e64 s[12:13], s6, v124
	v_addc_co_u32_e64 v8, s[20:21], 0, v8, s[16:17]
	v_cmp_le_u32_e64 s[16:17], s6, v125
	v_addc_co_u32_e64 v8, s[20:21], 0, v8, s[8:9]
	v_cmp_le_u32_e64 s[8:9], s6, v126
	v_addc_co_u32_e64 v8, s[20:21], 0, v8, s[12:13]
	v_cmp_le_u32_e64 s[12:13], s6, v127
	v_addc_co_u32_e64 v8, s[20:21], 0, v8, s[16:17]
	v_cmp_le_u32_e64 s[16:17], s6, v128
	v_addc_co_u32_e64 v8, s[20:21], 0, v8, s[8:9]
	v_cmp_le_u32_e64 s[8:9], s6, v129
	v_addc_co_u32_e64 v8, s[20:21], 0, v8, s[12:13]
	v_cmp_le_u32_e64 s[12:13], s6, v130
	v_addc_co_u32_e64 v8, s[20:21], 0, v8, s[16:17]
	v_cmp_le_u32_e64 s[16:17], s6, v132
	v_addc_co_u32_e64 v8, s[20:21], 0, v8, s[8:9]
	v_cmp_le_u32_e64 s[8:9], s6, v133
	v_addc_co_u32_e64 v8, s[20:21], 0, v8, s[12:13]
	v_addc_co_u32_e64 v8, s[20:21], 0, v8, s[16:17]
	v_addc_co_u32_e64 v8, s[20:21], 0, v8, s[8:9]
	v_and_b32_e32 v9, 16, v8
	v_cmp_ne_u32_e64 s[22:23], 0, v9
	v_and_b32_e32 v9, 8, v8
	v_cmp_ne_u32_e64 s[18:19], 0, v9
	v_and_b32_e32 v9, 4, v8
	v_cmp_ne_u32_e64 s[16:17], 0, v9
	v_and_b32_e32 v9, 2, v8
	v_cmp_ne_u32_e64 s[12:13], 0, v9
	v_and_b32_e32 v9, 1, v8
	v_cmp_ne_u32_e64 s[8:9], 0, v9
	s_bcnt1_i32_b64 s7, s[22:23]
	s_bcnt1_i32_b64 s3, s[18:19]
	s_lshl1_add_u32 s7, s7, s3
	s_bcnt1_i32_b64 s3, s[16:17]
	s_lshl1_add_u32 s7, s7, s3
	s_bcnt1_i32_b64 s3, s[12:13]
	s_lshl1_add_u32 s7, s7, s3
	s_bcnt1_i32_b64 s3, s[8:9]
	s_lshl1_add_u32 s7, s7, s3
	s_cmpk_lt_u32 s7, 0x100
	s_cselect_b32 s4, s4, s6
	s_cmpk_eq_u32 s7, 0x100
	s_cbranch_scc1 .Ltk2_x16
	s_lshr_b32 s5, s5, 1
	s_cbranch_scc1 .Ltk2_l16
	s_branch .Ltk2_orig
.Ltk2_l8:
	s_or_b32 s6, s4, s5
	v_cmp_le_u32_e64 s[8:9], s6, v111
	v_cmp_le_u32_e64 s[12:13], s6, v113
	v_cmp_le_u32_e64 s[16:17], s6, v115
	v_cndmask_b32_e64 v8, 0, 1, s[8:9]
	v_cmp_le_u32_e64 s[8:9], s6, v117
	v_addc_co_u32_e64 v8, s[20:21], 0, v8, s[12:13]
	v_cmp_le_u32_e64 s[12:13], s6, v119
	v_addc_co_u32_e64 v8, s[20:21], 0, v8, s[16:17]
	v_cmp_le_u32_e64 s[16:17], s6, v121
	v_addc_co_u32_e64 v8, s[20:21], 0, v8, s[8:9]
	v_cmp_le_u32_e64 s[8:9], s6, v123
	v_addc_co_u32_e64 v8, s[20:21], 0, v8, s[12:13]
	v_cmp_le_u32_e64 s[12:13], s6, v124
	v_addc_co_u32_e64 v8, s[20:21], 0, v8, s[16:17]
	v_addc_co_u32_e64 v8, s[20:21], 0, v8, s[8:9]
	v_addc_co_u32_e64 v8, s[20:21], 0, v8, s[12:13]
	v_and_b32_e32 v9, 8, v8
	v_cmp_ne_u32_e64 s[18:19], 0, v9
	v_and_b32_e32 v9, 4, v8
	v_cmp_ne_u32_e64 s[16:17], 0, v9
	v_and_b32_e32 v9, 2, v8
	v_cmp_ne_u32_e64 s[12:13], 0, v9
	v_and_b32_e32 v9, 1, v8
	v_cmp_ne_u32_e64 s[8:9], 0, v9
	s_bcnt1_i32_b64 s7, s[18:19]
	s_bcnt1_i32_b64 s3, s[16:17]
	s_lshl1_add_u32 s7, s7, s3
	s_bcnt1_i32_b64 s3, s[12:13]
	s_lshl1_add_u32 s7, s7, s3
	s_bcnt1_i32_b64 s3, s[8:9]
	s_lshl1_add_u32 s7, s7, s3
	s_cmpk_lt_u32 s7, 0x100
	s_cselect_b32 s4, s4, s6
	s_cmpk_eq_u32 s7, 0x100
	s_cbranch_scc1 .Ltk2_x8
	s_lshr_b32 s5, s5, 1
	s_cbranch_scc1 .Ltk2_l8
	s_branch .Ltk2_orig
.Ltk2_x32:
	v_cmp_le_u32_e64 s[8:9], s4, v111
	v_cmp_le_u32_e64 s[12:13], s4, v113
	v_cmp_le_u32_e64 s[16:17], s4, v115
	s_nop 0
	v_writelane_b32 v10, s8, 0
	v_writelane_b32 v11, s9, 0
	v_cmp_le_u32_e64 s[8:9], s4, v117
	v_writelane_b32 v10, s12, 1
	v_writelane_b32 v11, s13, 1
	v_cmp_le_u32_e64 s[12:13], s4, v119
	v_writelane_b32 v10, s16, 2
	v_writelane_b32 v11, s17, 2
	v_cmp_le_u32_e64 s[16:17], s4, v121
	v_writelane_b32 v10, s8, 3
	v_writelane_b32 v11, s9, 3
	v_cmp_le_u32_e64 s[8:9], s4, v123
	v_writelane_b32 v10, s12, 4
	v_writelane_b32 v11, s13, 4
	v_cmp_le_u32_e64 s[12:13], s4, v124
	v_writelane_b32 v10, s16, 5
	v_writelane_b32 v11, s17, 5
	v_cmp_le_u32_e64 s[16:17], s4, v125
	v_writelane_b32 v10, s8, 6
	v_writelane_b32 v11, s9, 6
	v_cmp_le_u32_e64 s[8:9], s4, v126
	v_writelane_b32 v10, s12, 7
	v_writelane_b32 v11, s13, 7
	v_cmp_le_u32_e64 s[12:13], s4, v127
	v_writelane_b32 v10, s16, 8
	v_writelane_b32 v11, s17, 8
	v_cmp_le_u32_e64 s[16:17], s4, v128
	v_writelane_b32 v10, s8, 9
	v_writelane_b32 v11, s9, 9
	v_cmp_le_u32_e64 s[8:9], s4, v129
	v_writelane_b32 v10, s12, 10
	v_writelane_b32 v11, s13, 10
	v_cmp_le_u32_e64 s[12:13], s4, v130
	v_writelane_b32 v10, s16, 11
	v_writelane_b32 v11, s17, 11
	v_cmp_le_u32_e64 s[16:17], s4, v132
	v_writelane_b32 v10, s8, 12
	v_writelane_b32 v11, s9, 12
	v_cmp_le_u32_e64 s[8:9], s4, v133
	v_writelane_b32 v10, s12, 13
	v_writelane_b32 v11, s13, 13
	v_cmp_le_u32_e64 s[12:13], s4, v138
	v_writelane_b32 v10, s16, 14
	v_writelane_b32 v11, s17, 14
	v_cmp_le_u32_e64 s[16:17], s4, v139
	v_writelane_b32 v10, s8, 15
	v_writelane_b32 v11, s9, 15
	v_cmp_le_u32_e64 s[8:9], s4, v141
	v_writelane_b32 v10, s12, 16
	v_writelane_b32 v11, s13, 16
	v_cmp_le_u32_e64 s[12:13], s4, v143
	v_writelane_b32 v10, s16, 17
	v_writelane_b32 v11, s17, 17
	v_cmp_le_u32_e64 s[16:17], s4, v145
	v_writelane_b32 v10, s8, 18
	v_writelane_b32 v11, s9, 18
	v_cmp_le_u32_e64 s[8:9], s4, v147
	v_writelane_b32 v10, s12, 19
	v_writelane_b32 v11, s13, 19
	v_cmp_le_u32_e64 s[12:13], s4, v149
	v_writelane_b32 v10, s16, 20
	v_writelane_b32 v11, s17, 20
	v_cmp_le_u32_e64 s[16:17], s4, v151
	v_writelane_b32 v10, s8, 21
	v_writelane_b32 v11, s9, 21
	v_cmp_le_u32_e64 s[8:9], s4, v160
	v_writelane_b32 v10, s12, 22
	v_writelane_b32 v11, s13, 22
	v_cmp_le_u32_e64 s[12:13], s4, v163
	v_writelane_b32 v10, s16, 23
	v_writelane_b32 v11, s17, 23
	v_cmp_le_u32_e64 s[16:17], s4, v165
	v_writelane_b32 v10, s8, 24
	v_writelane_b32 v11, s9, 24
	v_cmp_le_u32_e64 s[8:9], s4, v166
	v_writelane_b32 v10, s12, 25
	v_writelane_b32 v11, s13, 25
	v_cmp_le_u32_e64 s[12:13], s4, v167
	v_writelane_b32 v10, s16, 26
	v_writelane_b32 v11, s17, 26
	v_cmp_le_u32_e64 s[16:17], s4, v168
	v_writelane_b32 v10, s8, 27
	v_writelane_b32 v11, s9, 27
	v_cmp_le_u32_e64 s[8:9], s4, v169
	v_writelane_b32 v10, s12, 28
	v_writelane_b32 v11, s13, 28
	v_cmp_le_u32_e64 s[12:13], s4, v6
	v_writelane_b32 v10, s16, 29
	v_writelane_b32 v11, s17, 29
	v_writelane_b32 v10, s8, 30
	v_writelane_b32 v11, s9, 30
	v_writelane_b32 v10, s12, 31
	v_writelane_b32 v11, s13, 31
	v_mov_b32_e32 v2, v10
	v_mov_b32_e32 v3, v11
	s_branch .LBB0_2415
.Ltk2_x24:
	v_cmp_le_u32_e64 s[8:9], s4, v111
	v_cmp_le_u32_e64 s[12:13], s4, v113
	v_cmp_le_u32_e64 s[16:17], s4, v115
	s_nop 0
	v_writelane_b32 v10, s8, 0
	v_writelane_b32 v11, s9, 0
	v_cmp_le_u32_e64 s[8:9], s4, v117
	v_writelane_b32 v10, s12, 1
	v_writelane_b32 v11, s13, 1
	v_cmp_le_u32_e64 s[12:13], s4, v119
	v_writelane_b32 v10, s16, 2
	v_writelane_b32 v11, s17, 2
	v_cmp_le_u32_e64 s[16:17], s4, v121
	v_writelane_b32 v10, s8, 3
	v_writelane_b32 v11, s9, 3
	v_cmp_le_u32_e64 s[8:9], s4, v123
	v_writelane_b32 v10, s12, 4
	v_writelane_b32 v11, s13, 4
	v_cmp_le_u32_e64 s[12:13], s4, v124
	v_writelane_b32 v10, s16, 5
	v_writelane_b32 v11, s17, 5
	v_cmp_le_u32_e64 s[16:17], s4, v125
	v_writelane_b32 v10, s8, 6
	v_writelane_b32 v11, s9, 6
	v_cmp_le_u32_e64 s[8:9], s4, v126
	v_writelane_b32 v10, s12, 7
	v_writelane_b32 v11, s13, 7
	v_cmp_le_u32_e64 s[12:13], s4, v127
	v_writelane_b32 v10, s16, 8
	v_writelane_b32 v11, s17, 8
	v_cmp_le_u32_e64 s[16:17], s4, v128
	v_writelane_b32 v10, s8, 9
	v_writelane_b32 v11, s9, 9
	v_cmp_le_u32_e64 s[8:9], s4, v129
	v_writelane_b32 v10, s12, 10
	v_writelane_b32 v11, s13, 10
	v_cmp_le_u32_e64 s[12:13], s4, v130
	v_writelane_b32 v10, s16, 11
	v_writelane_b32 v11, s17, 11
	v_cmp_le_u32_e64 s[16:17], s4, v132
	v_writelane_b32 v10, s8, 12
	v_writelane_b32 v11, s9, 12
	v_cmp_le_u32_e64 s[8:9], s4, v133
	v_writelane_b32 v10, s12, 13
	v_writelane_b32 v11, s13, 13
	v_cmp_le_u32_e64 s[12:13], s4, v138
	v_writelane_b32 v10, s16, 14
	v_writelane_b32 v11, s17, 14
	v_cmp_le_u32_e64 s[16:17], s4, v139
	v_writelane_b32 v10, s8, 15
	v_writelane_b32 v11, s9, 15
	v_cmp_le_u32_e64 s[8:9], s4, v141
	v_writelane_b32 v10, s12, 16
	v_writelane_b32 v11, s13, 16
	v_cmp_le_u32_e64 s[12:13], s4, v143
	v_writelane_b32 v10, s16, 17
	v_writelane_b32 v11, s17, 17
	v_cmp_le_u32_e64 s[16:17], s4, v145
	v_writelane_b32 v10, s8, 18
	v_writelane_b32 v11, s9, 18
	v_cmp_le_u32_e64 s[8:9], s4, v147
	v_writelane_b32 v10, s12, 19
	v_writelane_b32 v11, s13, 19
	v_cmp_le_u32_e64 s[12:13], s4, v149
	v_writelane_b32 v10, s16, 20
	v_writelane_b32 v11, s17, 20
	v_cmp_le_u32_e64 s[16:17], s4, v151
	v_writelane_b32 v10, s8, 21
	v_writelane_b32 v11, s9, 21
	v_writelane_b32 v10, s12, 22
	v_writelane_b32 v11, s13, 22
	v_writelane_b32 v10, s16, 23
	v_writelane_b32 v11, s17, 23
	v_mov_b32_e32 v2, v10
	v_mov_b32_e32 v3, v11
	s_branch .LBB0_2415
.Ltk2_x16:
	v_cmp_le_u32_e64 s[8:9], s4, v111
	v_cmp_le_u32_e64 s[12:13], s4, v113
	v_cmp_le_u32_e64 s[16:17], s4, v115
	s_nop 0
	v_writelane_b32 v10, s8, 0
	v_writelane_b32 v11, s9, 0
	v_cmp_le_u32_e64 s[8:9], s4, v117
	v_writelane_b32 v10, s12, 1
	v_writelane_b32 v11, s13, 1
	v_cmp_le_u32_e64 s[12:13], s4, v119
	v_writelane_b32 v10, s16, 2
	v_writelane_b32 v11, s17, 2
	v_cmp_le_u32_e64 s[16:17], s4, v121
	v_writelane_b32 v10, s8, 3
	v_writelane_b32 v11, s9, 3
	v_cmp_le_u32_e64 s[8:9], s4, v123
	v_writelane_b32 v10, s12, 4
	v_writelane_b32 v11, s13, 4
	v_cmp_le_u32_e64 s[12:13], s4, v124
	v_writelane_b32 v10, s16, 5
	v_writelane_b32 v11, s17, 5
	v_cmp_le_u32_e64 s[16:17], s4, v125
	v_writelane_b32 v10, s8, 6
	v_writelane_b32 v11, s9, 6
	v_cmp_le_u32_e64 s[8:9], s4, v126
	v_writelane_b32 v10, s12, 7
	v_writelane_b32 v11, s13, 7
	v_cmp_le_u32_e64 s[12:13], s4, v127
	v_writelane_b32 v10, s16, 8
	v_writelane_b32 v11, s17, 8
	v_cmp_le_u32_e64 s[16:17], s4, v128
	v_writelane_b32 v10, s8, 9
	v_writelane_b32 v11, s9, 9
	v_cmp_le_u32_e64 s[8:9], s4, v129
	v_writelane_b32 v10, s12, 10
	v_writelane_b32 v11, s13, 10
	v_cmp_le_u32_e64 s[12:13], s4, v130
	v_writelane_b32 v10, s16, 11
	v_writelane_b32 v11, s17, 11
	v_cmp_le_u32_e64 s[16:17], s4, v132
	v_writelane_b32 v10, s8, 12
	v_writelane_b32 v11, s9, 12
	v_cmp_le_u32_e64 s[8:9], s4, v133
	v_writelane_b32 v10, s12, 13
	v_writelane_b32 v11, s13, 13
	v_writelane_b32 v10, s16, 14
	v_writelane_b32 v11, s17, 14
	v_writelane_b32 v10, s8, 15
	v_writelane_b32 v11, s9, 15
	v_mov_b32_e32 v2, v10
	v_mov_b32_e32 v3, v11
	s_branch .LBB0_2415
.Ltk2_x8:
	v_cmp_le_u32_e64 s[8:9], s4, v111
	v_cmp_le_u32_e64 s[12:13], s4, v113
	v_cmp_le_u32_e64 s[16:17], s4, v115
	s_nop 0
	v_writelane_b32 v10, s8, 0
	v_writelane_b32 v11, s9, 0
	v_cmp_le_u32_e64 s[8:9], s4, v117
	v_writelane_b32 v10, s12, 1
	v_writelane_b32 v11, s13, 1
	v_cmp_le_u32_e64 s[12:13], s4, v119
	v_writelane_b32 v10, s16, 2
	v_writelane_b32 v11, s17, 2
	v_cmp_le_u32_e64 s[16:17], s4, v121
	v_writelane_b32 v10, s8, 3
	v_writelane_b32 v11, s9, 3
	v_cmp_le_u32_e64 s[8:9], s4, v123
	v_writelane_b32 v10, s12, 4
	v_writelane_b32 v11, s13, 4
	v_cmp_le_u32_e64 s[12:13], s4, v124
	v_writelane_b32 v10, s16, 5
	v_writelane_b32 v11, s17, 5
	v_writelane_b32 v10, s8, 6
	v_writelane_b32 v11, s9, 6
	v_writelane_b32 v10, s12, 7
	v_writelane_b32 v11, s13, 7
	v_mov_b32_e32 v2, v10
	v_mov_b32_e32 v3, v11
	s_branch .LBB0_2415

.Ltk3_l32:
	s_or_b32 s6, s4, s5
	v_cmp_le_u32_e64 s[8:9], s6, v93
	v_cmp_le_u32_e64 s[12:13], s6, v94
	v_cmp_le_u32_e64 s[16:17], s6, v95
	v_cndmask_b32_e64 v8, 0, 1, s[8:9]
	v_cmp_le_u32_e64 s[8:9], s6, v96
	v_addc_co_u32_e64 v8, s[20:21], 0, v8, s[12:13]
	v_cmp_le_u32_e64 s[12:13], s6, v97
	v_addc_co_u32_e64 v8, s[20:21], 0, v8, s[16:17]
	v_cmp_le_u32_e64 s[16:17], s6, v98
	v_addc_co_u32_e64 v8, s[20:21], 0, v8, s[8:9]
	v_cmp_le_u32_e64 s[8:9], s6, v99
	v_addc_co_u32_e64 v8, s[20:21], 0, v8, s[12:13]
	v_cmp_le_u32_e64 s[12:13], s6, v100
	v_addc_co_u32_e64 v8, s[20:21], 0, v8, s[16:17]
	v_cmp_le_u32_e64 s[16:17], s6, v101
	v_addc_co_u32_e64 v8, s[20:21], 0, v8, s[8:9]
	v_cmp_le_u32_e64 s[8:9], s6, v102
	v_addc_co_u32_e64 v8, s[20:21], 0, v8, s[12:13]
	v_cmp_le_u32_e64 s[12:13], s6, v103
	v_addc_co_u32_e64 v8, s[20:21], 0, v8, s[16:17]
	v_cmp_le_u32_e64 s[16:17], s6, v104
	v_addc_co_u32_e64 v8, s[20:21], 0, v8, s[8:9]
	v_cmp_le_u32_e64 s[8:9], s6, v105
	v_addc_co_u32_e64 v8, s[20:21], 0, v8, s[12:13]
	v_cmp_le_u32_e64 s[12:13], s6, v106
	v_addc_co_u32_e64 v8, s[20:21], 0, v8, s[16:17]
	v_cmp_le_u32_e64 s[16:17], s6, v107
	v_addc_co_u32_e64 v8, s[20:21], 0, v8, s[8:9]
	v_cmp_le_u32_e64 s[8:9], s6, v108
	v_addc_co_u32_e64 v8, s[20:21], 0, v8, s[12:13]
	v_cmp_le_u32_e64 s[12:13], s6, v109
	v_addc_co_u32_e64 v8, s[20:21], 0, v8, s[16:17]
	v_cmp_le_u32_e64 s[16:17], s6, v110
	v_addc_co_u32_e64 v8, s[20:21], 0, v8, s[8:9]
	v_cmp_le_u32_e64 s[8:9], s6, v112
	v_addc_co_u32_e64 v8, s[20:21], 0, v8, s[12:13]
	v_cmp_le_u32_e64 s[12:13], s6, v114
	v_addc_co_u32_e64 v8, s[20:21], 0, v8, s[16:17]
	v_cmp_le_u32_e64 s[16:17], s6, v116
	v_addc_co_u32_e64 v8, s[20:21], 0, v8, s[8:9]
	v_cmp_le_u32_e64 s[8:9], s6, v118
	v_addc_co_u32_e64 v8, s[20:21], 0, v8, s[12:13]
	v_cmp_le_u32_e64 s[12:13], s6, v120
	v_addc_co_u32_e64 v8, s[20:21], 0, v8, s[16:17]
	v_cmp_le_u32_e64 s[16:17], s6, v122
	v_addc_co_u32_e64 v8, s[20:21], 0, v8, s[8:9]
	v_cmp_le_u32_e64 s[8:9], s6, v131
	v_addc_co_u32_e64 v8, s[20:21], 0, v8, s[12:13]
	v_cmp_le_u32_e64 s[12:13], s6, v90
	v_addc_co_u32_e64 v8, s[20:21], 0, v8, s[16:17]
	v_cmp_le_u32_e64 s[16:17], s6, v91
	v_addc_co_u32_e64 v8, s[20:21], 0, v8, s[8:9]
	v_cmp_le_u32_e64 s[8:9], s6, v134
	v_addc_co_u32_e64 v8, s[20:21], 0, v8, s[12:13]
	v_cmp_le_u32_e64 s[12:13], s6, v135
	v_addc_co_u32_e64 v8, s[20:21], 0, v8, s[16:17]
	v_cmp_le_u32_e64 s[16:17], s6, v136
	v_addc_co_u32_e64 v8, s[20:21], 0, v8, s[8:9]
	v_cmp_le_u32_e64 s[8:9], s6, v137
	v_addc_co_u32_e64 v8, s[20:21], 0, v8, s[12:13]
	v_cmp_le_u32_e64 s[12:13], s6, v4
	v_addc_co_u32_e64 v8, s[20:21], 0, v8, s[16:17]
	v_addc_co_u32_e64 v8, s[20:21], 0, v8, s[8:9]
	v_addc_co_u32_e64 v8, s[20:21], 0, v8, s[12:13]
	v_and_b32_e32 v9, 32, v8
	v_cmp_ne_u32_e64 s[0:1], 0, v9
	v_and_b32_e32 v9, 16, v8
	v_cmp_ne_u32_e64 s[22:23], 0, v9
	v_and_b32_e32 v9, 8, v8
	v_cmp_ne_u32_e64 s[18:19], 0, v9
	v_and_b32_e32 v9, 4, v8
	v_cmp_ne_u32_e64 s[16:17], 0, v9
	v_and_b32_e32 v9, 2, v8
	v_cmp_ne_u32_e64 s[12:13], 0, v9
	v_and_b32_e32 v9, 1, v8
	v_cmp_ne_u32_e64 s[8:9], 0, v9
	s_bcnt1_i32_b64 s7, s[0:1]
	s_bcnt1_i32_b64 s3, s[22:23]
	s_lshl1_add_u32 s7, s7, s3
	s_bcnt1_i32_b64 s3, s[18:19]
	s_lshl1_add_u32 s7, s7, s3
	s_bcnt1_i32_b64 s3, s[16:17]
	s_lshl1_add_u32 s7, s7, s3
	s_bcnt1_i32_b64 s3, s[12:13]
	s_lshl1_add_u32 s7, s7, s3
	s_bcnt1_i32_b64 s3, s[8:9]
	s_lshl1_add_u32 s7, s7, s3
	s_cmpk_lt_u32 s7, 0x100
	s_cselect_b32 s4, s4, s6
	s_cmpk_eq_u32 s7, 0x100
	s_cbranch_scc1 .Ltk3_x32
	s_lshr_b32 s5, s5, 1
	s_cbranch_scc1 .Ltk3_l32
	s_branch .Ltk3_orig
.Ltk3_l24:
	s_or_b32 s6, s4, s5
	v_cmp_le_u32_e64 s[8:9], s6, v93
	v_cmp_le_u32_e64 s[12:13], s6, v94
	v_cmp_le_u32_e64 s[16:17], s6, v95
	v_cndmask_b32_e64 v8, 0, 1, s[8:9]
	v_cmp_le_u32_e64 s[8:9], s6, v96
	v_addc_co_u32_e64 v8, s[20:21], 0, v8, s[12:13]
	v_cmp_le_u32_e64 s[12:13], s6, v97
	v_addc_co_u32_e64 v8, s[20:21], 0, v8, s[16:17]
	v_cmp_le_u32_e64 s[16:17], s6, v98
	v_addc_co_u32_e64 v8, s[20:21], 0, v8, s[8:9]
	v_cmp_le_u32_e64 s[8:9], s6, v99
	v_addc_co_u32_e64 v8, s[20:21], 0, v8, s[12:13]
	v_cmp_le_u32_e64 s[12:13], s6, v100
	v_addc_co_u32_e64 v8, s[20:21], 0, v8, s[16:17]
	v_cmp_le_u32_e64 s[16:17], s6, v101
	v_addc_co_u32_e64 v8, s[20:21], 0, v8, s[8:9]
	v_cmp_le_u32_e64 s[8:9], s6, v102
	v_addc_co_u32_e64 v8, s[20:21], 0, v8, s[12:13]
	v_cmp_le_u32_e64 s[12:13], s6, v103
	v_addc_co_u32_e64 v8, s[20:21], 0, v8, s[16:17]
	v_cmp_le_u32_e64 s[16:17], s6, v104
	v_addc_co_u32_e64 v8, s[20:21], 0, v8, s[8:9]
	v_cmp_le_u32_e64 s[8:9], s6, v105
	v_addc_co_u32_e64 v8, s[20:21], 0, v8, s[12:13]
	v_cmp_le_u32_e64 s[12:13], s6, v106
	v_addc_co_u32_e64 v8, s[20:21], 0, v8, s[16:17]
	v_cmp_le_u32_e64 s[16:17], s6, v107
	v_addc_co_u32_e64 v8, s[20:21], 0, v8, s[8:9]
	v_cmp_le_u32_e64 s[8:9], s6, v108
	v_addc_co_u32_e64 v8, s[20:21], 0, v8, s[12:13]
	v_cmp_le_u32_e64 s[12:13], s6, v109
	v_addc_co_u32_e64 v8, s[20:21], 0, v8, s[16:17]
	v_cmp_le_u32_e64 s[16:17], s6, v110
	v_addc_co_u32_e64 v8, s[20:21], 0, v8, s[8:9]
	v_cmp_le_u32_e64 s[8:9], s6, v112
	v_addc_co_u32_e64 v8, s[20:21], 0, v8, s[12:13]
	v_cmp_le_u32_e64 s[12:13], s6, v114
	v_addc_co_u32_e64 v8, s[20:21], 0, v8, s[16:17]
	v_cmp_le_u32_e64 s[16:17], s6, v116
	v_addc_co_u32_e64 v8, s[20:21], 0, v8, s[8:9]
	v_cmp_le_u32_e64 s[8:9], s6, v118
	v_addc_co_u32_e64 v8, s[20:21], 0, v8, s[12:13]
	v_cmp_le_u32_e64 s[12:13], s6, v120
	v_addc_co_u32_e64 v8, s[20:21], 0, v8, s[16:17]
	v_cmp_le_u32_e64 s[16:17], s6, v122
	v_addc_co_u32_e64 v8, s[20:21], 0, v8, s[8:9]
	v_addc_co_u32_e64 v8, s[20:21], 0, v8, s[12:13]
	v_addc_co_u32_e64 v8, s[20:21], 0, v8, s[16:17]
	v_and_b32_e32 v9, 16, v8
	v_cmp_ne_u32_e64 s[22:23], 0, v9
	v_and_b32_e32 v9, 8, v8
	v_cmp_ne_u32_e64 s[18:19], 0, v9
	v_and_b32_e32 v9, 4, v8
	v_cmp_ne_u32_e64 s[16:17], 0, v9
	v_and_b32_e32 v9, 2, v8
	v_cmp_ne_u32_e64 s[12:13], 0, v9
	v_and_b32_e32 v9, 1, v8
	v_cmp_ne_u32_e64 s[8:9], 0, v9
	s_bcnt1_i32_b64 s7, s[22:23]
	s_bcnt1_i32_b64 s3, s[18:19]
	s_lshl1_add_u32 s7, s7, s3
	s_bcnt1_i32_b64 s3, s[16:17]
	s_lshl1_add_u32 s7, s7, s3
	s_bcnt1_i32_b64 s3, s[12:13]
	s_lshl1_add_u32 s7, s7, s3
	s_bcnt1_i32_b64 s3, s[8:9]
	s_lshl1_add_u32 s7, s7, s3
	s_cmpk_lt_u32 s7, 0x100
	s_cselect_b32 s4, s4, s6
	s_cmpk_eq_u32 s7, 0x100
	s_cbranch_scc1 .Ltk3_x24
	s_lshr_b32 s5, s5, 1
	s_cbranch_scc1 .Ltk3_l24
	s_branch .Ltk3_orig
.Ltk3_l16:
	s_or_b32 s6, s4, s5
	v_cmp_le_u32_e64 s[8:9], s6, v93
	v_cmp_le_u32_e64 s[12:13], s6, v94
	v_cmp_le_u32_e64 s[16:17], s6, v95
	v_cndmask_b32_e64 v8, 0, 1, s[8:9]
	v_cmp_le_u32_e64 s[8:9], s6, v96
	v_addc_co_u32_e64 v8, s[20:21], 0, v8, s[12:13]
	v_cmp_le_u32_e64 s[12:13], s6, v97
	v_addc_co_u32_e64 v8, s[20:21], 0, v8, s[16:17]
	v_cmp_le_u32_e64 s[16:17], s6, v98
	v_addc_co_u32_e64 v8, s[20:21], 0, v8, s[8:9]
	v_cmp_le_u32_e64 s[8:9], s6, v99
	v_addc_co_u32_e64 v8, s[20:21], 0, v8, s[12:13]
	v_cmp_le_u32_e64 s[12:13], s6, v100
	v_addc_co_u32_e64 v8, s[20:21], 0, v8, s[16:17]
	v_cmp_le_u32_e64 s[16:17], s6, v101
	v_addc_co_u32_e64 v8, s[20:21], 0, v8, s[8:9]
	v_cmp_le_u32_e64 s[8:9], s6, v102
	v_addc_co_u32_e64 v8, s[20:21], 0, v8, s[12:13]
	v_cmp_le_u32_e64 s[12:13], s6, v103
	v_addc_co_u32_e64 v8, s[20:21], 0, v8, s[16:17]
	v_cmp_le_u32_e64 s[16:17], s6, v104
	v_addc_co_u32_e64 v8, s[20:21], 0, v8, s[8:9]
	v_cmp_le_u32_e64 s[8:9], s6, v105
	v_addc_co_u32_e64 v8, s[20:21], 0, v8, s[12:13]
	v_cmp_le_u32_e64 s[12:13], s6, v106
	v_addc_co_u32_e64 v8, s[20:21], 0, v8, s[16:17]
	v_cmp_le_u32_e64 s[16:17], s6, v107
	v_addc_co_u32_e64 v8, s[20:21], 0, v8, s[8:9]
	v_cmp_le_u32_e64 s[8:9], s6, v108
	v_addc_co_u32_e64 v8, s[20:21], 0, v8, s[12:13]
	v_addc_co_u32_e64 v8, s[20:21], 0, v8, s[16:17]
	v_addc_co_u32_e64 v8, s[20:21], 0, v8, s[8:9]
	v_and_b32_e32 v9, 16, v8
	v_cmp_ne_u32_e64 s[22:23], 0, v9
	v_and_b32_e32 v9, 8, v8
	v_cmp_ne_u32_e64 s[18:19], 0, v9
	v_and_b32_e32 v9, 4, v8
	v_cmp_ne_u32_e64 s[16:17], 0, v9
	v_and_b32_e32 v9, 2, v8
	v_cmp_ne_u32_e64 s[12:13], 0, v9
	v_and_b32_e32 v9, 1, v8
	v_cmp_ne_u32_e64 s[8:9], 0, v9
	s_bcnt1_i32_b64 s7, s[22:23]
	s_bcnt1_i32_b64 s3, s[18:19]
	s_lshl1_add_u32 s7, s7, s3
	s_bcnt1_i32_b64 s3, s[16:17]
	s_lshl1_add_u32 s7, s7, s3
	s_bcnt1_i32_b64 s3, s[12:13]
	s_lshl1_add_u32 s7, s7, s3
	s_bcnt1_i32_b64 s3, s[8:9]
	s_lshl1_add_u32 s7, s7, s3
	s_cmpk_lt_u32 s7, 0x100
	s_cselect_b32 s4, s4, s6
	s_cmpk_eq_u32 s7, 0x100
	s_cbranch_scc1 .Ltk3_x16
	s_lshr_b32 s5, s5, 1
	s_cbranch_scc1 .Ltk3_l16
	s_branch .Ltk3_orig
.Ltk3_l8:
	s_or_b32 s6, s4, s5
	v_cmp_le_u32_e64 s[8:9], s6, v93
	v_cmp_le_u32_e64 s[12:13], s6, v94
	v_cmp_le_u32_e64 s[16:17], s6, v95
	v_cndmask_b32_e64 v8, 0, 1, s[8:9]
	v_cmp_le_u32_e64 s[8:9], s6, v96
	v_addc_co_u32_e64 v8, s[20:21], 0, v8, s[12:13]
	v_cmp_le_u32_e64 s[12:13], s6, v97
	v_addc_co_u32_e64 v8, s[20:21], 0, v8, s[16:17]
	v_cmp_le_u32_e64 s[16:17], s6, v98
	v_addc_co_u32_e64 v8, s[20:21], 0, v8, s[8:9]
	v_cmp_le_u32_e64 s[8:9], s6, v99
	v_addc_co_u32_e64 v8, s[20:21], 0, v8, s[12:13]
	v_cmp_le_u32_e64 s[12:13], s6, v100
	v_addc_co_u32_e64 v8, s[20:21], 0, v8, s[16:17]
	v_addc_co_u32_e64 v8, s[20:21], 0, v8, s[8:9]
	v_addc_co_u32_e64 v8, s[20:21], 0, v8, s[12:13]
	v_and_b32_e32 v9, 8, v8
	v_cmp_ne_u32_e64 s[18:19], 0, v9
	v_and_b32_e32 v9, 4, v8
	v_cmp_ne_u32_e64 s[16:17], 0, v9
	v_and_b32_e32 v9, 2, v8
	v_cmp_ne_u32_e64 s[12:13], 0, v9
	v_and_b32_e32 v9, 1, v8
	v_cmp_ne_u32_e64 s[8:9], 0, v9
	s_bcnt1_i32_b64 s7, s[18:19]
	s_bcnt1_i32_b64 s3, s[16:17]
	s_lshl1_add_u32 s7, s7, s3
	s_bcnt1_i32_b64 s3, s[12:13]
	s_lshl1_add_u32 s7, s7, s3
	s_bcnt1_i32_b64 s3, s[8:9]
	s_lshl1_add_u32 s7, s7, s3
	s_cmpk_lt_u32 s7, 0x100
	s_cselect_b32 s4, s4, s6
	s_cmpk_eq_u32 s7, 0x100
	s_cbranch_scc1 .Ltk3_x8
	s_lshr_b32 s5, s5, 1
	s_cbranch_scc1 .Ltk3_l8
	s_branch .Ltk3_orig
.Ltk3_x32:
	v_cmp_le_u32_e64 s[8:9], s4, v93
	v_cmp_le_u32_e64 s[12:13], s4, v94
	v_cmp_le_u32_e64 s[16:17], s4, v95
	s_nop 0
	v_writelane_b32 v10, s8, 0
	v_writelane_b32 v11, s9, 0
	v_cmp_le_u32_e64 s[8:9], s4, v96
	v_writelane_b32 v10, s12, 1
	v_writelane_b32 v11, s13, 1
	v_cmp_le_u32_e64 s[12:13], s4, v97
	v_writelane_b32 v10, s16, 2
	v_writelane_b32 v11, s17, 2
	v_cmp_le_u32_e64 s[16:17], s4, v98
	v_writelane_b32 v10, s8, 3
	v_writelane_b32 v11, s9, 3
	v_cmp_le_u32_e64 s[8:9], s4, v99
	v_writelane_b32 v10, s12, 4
	v_writelane_b32 v11, s13, 4
	v_cmp_le_u32_e64 s[12:13], s4, v100
	v_writelane_b32 v10, s16, 5
	v_writelane_b32 v11, s17, 5
	v_cmp_le_u32_e64 s[16:17], s4, v101
	v_writelane_b32 v10, s8, 6
	v_writelane_b32 v11, s9, 6
	v_cmp_le_u32_e64 s[8:9], s4, v102
	v_writelane_b32 v10, s12, 7
	v_writelane_b32 v11, s13, 7
	v_cmp_le_u32_e64 s[12:13], s4, v103
	v_writelane_b32 v10, s16, 8
	v_writelane_b32 v11, s17, 8
	v_cmp_le_u32_e64 s[16:17], s4, v104
	v_writelane_b32 v10, s8, 9
	v_writelane_b32 v11, s9, 9
	v_cmp_le_u32_e64 s[8:9], s4, v105
	v_writelane_b32 v10, s12, 10
	v_writelane_b32 v11, s13, 10
	v_cmp_le_u32_e64 s[12:13], s4, v106
	v_writelane_b32 v10, s16, 11
	v_writelane_b32 v11, s17, 11
	v_cmp_le_u32_e64 s[16:17], s4, v107
	v_writelane_b32 v10, s8, 12
	v_writelane_b32 v11, s9, 12
	v_cmp_le_u32_e64 s[8:9], s4, v108
	v_writelane_b32 v10, s12, 13
	v_writelane_b32 v11, s13, 13
	v_cmp_le_u32_e64 s[12:13], s4, v109
	v_writelane_b32 v10, s16, 14
	v_writelane_b32 v11, s17, 14
	v_cmp_le_u32_e64 s[16:17], s4, v110
	v_writelane_b32 v10, s8, 15
	v_writelane_b32 v11, s9, 15
	v_cmp_le_u32_e64 s[8:9], s4, v112
	v_writelane_b32 v10, s12, 16
	v_writelane_b32 v11, s13, 16
	v_cmp_le_u32_e64 s[12:13], s4, v114
	v_writelane_b32 v10, s16, 17
	v_writelane_b32 v11, s17, 17
	v_cmp_le_u32_e64 s[16:17], s4, v116
	v_writelane_b32 v10, s8, 18
	v_writelane_b32 v11, s9, 18
	v_cmp_le_u32_e64 s[8:9], s4, v118
	v_writelane_b32 v10, s12, 19
	v_writelane_b32 v11, s13, 19
	v_cmp_le_u32_e64 s[12:13], s4, v120
	v_writelane_b32 v10, s16, 20
	v_writelane_b32 v11, s17, 20
	v_cmp_le_u32_e64 s[16:17], s4, v122
	v_writelane_b32 v10, s8, 21
	v_writelane_b32 v11, s9, 21
	v_cmp_le_u32_e64 s[8:9], s4, v131
	v_writelane_b32 v10, s12, 22
	v_writelane_b32 v11, s13, 22
	v_cmp_le_u32_e64 s[12:13], s4, v90
	v_writelane_b32 v10, s16, 23
	v_writelane_b32 v11, s17, 23
	v_cmp_le_u32_e64 s[16:17], s4, v91
	v_writelane_b32 v10, s8, 24
	v_writelane_b32 v11, s9, 24
	v_cmp_le_u32_e64 s[8:9], s4, v134
	v_writelane_b32 v10, s12, 25
	v_writelane_b32 v11, s13, 25
	v_cmp_le_u32_e64 s[12:13], s4, v135
	v_writelane_b32 v10, s16, 26
	v_writelane_b32 v11, s17, 26
	v_cmp_le_u32_e64 s[16:17], s4, v136
	v_writelane_b32 v10, s8, 27
	v_writelane_b32 v11, s9, 27
	v_cmp_le_u32_e64 s[8:9], s4, v137
	v_writelane_b32 v10, s12, 28
	v_writelane_b32 v11, s13, 28
	v_cmp_le_u32_e64 s[12:13], s4, v4
	v_writelane_b32 v10, s16, 29
	v_writelane_b32 v11, s17, 29
	v_writelane_b32 v10, s8, 30
	v_writelane_b32 v11, s9, 30
	v_writelane_b32 v10, s12, 31
	v_writelane_b32 v11, s13, 31
	v_mov_b32_e32 v2, v10
	v_mov_b32_e32 v3, v11
	s_branch .LBB0_2681
.Ltk3_x24:
	v_cmp_le_u32_e64 s[8:9], s4, v93
	v_cmp_le_u32_e64 s[12:13], s4, v94
	v_cmp_le_u32_e64 s[16:17], s4, v95
	s_nop 0
	v_writelane_b32 v10, s8, 0
	v_writelane_b32 v11, s9, 0
	v_cmp_le_u32_e64 s[8:9], s4, v96
	v_writelane_b32 v10, s12, 1
	v_writelane_b32 v11, s13, 1
	v_cmp_le_u32_e64 s[12:13], s4, v97
	v_writelane_b32 v10, s16, 2
	v_writelane_b32 v11, s17, 2
	v_cmp_le_u32_e64 s[16:17], s4, v98
	v_writelane_b32 v10, s8, 3
	v_writelane_b32 v11, s9, 3
	v_cmp_le_u32_e64 s[8:9], s4, v99
	v_writelane_b32 v10, s12, 4
	v_writelane_b32 v11, s13, 4
	v_cmp_le_u32_e64 s[12:13], s4, v100
	v_writelane_b32 v10, s16, 5
	v_writelane_b32 v11, s17, 5
	v_cmp_le_u32_e64 s[16:17], s4, v101
	v_writelane_b32 v10, s8, 6
	v_writelane_b32 v11, s9, 6
	v_cmp_le_u32_e64 s[8:9], s4, v102
	v_writelane_b32 v10, s12, 7
	v_writelane_b32 v11, s13, 7
	v_cmp_le_u32_e64 s[12:13], s4, v103
	v_writelane_b32 v10, s16, 8
	v_writelane_b32 v11, s17, 8
	v_cmp_le_u32_e64 s[16:17], s4, v104
	v_writelane_b32 v10, s8, 9
	v_writelane_b32 v11, s9, 9
	v_cmp_le_u32_e64 s[8:9], s4, v105
	v_writelane_b32 v10, s12, 10
	v_writelane_b32 v11, s13, 10
	v_cmp_le_u32_e64 s[12:13], s4, v106
	v_writelane_b32 v10, s16, 11
	v_writelane_b32 v11, s17, 11
	v_cmp_le_u32_e64 s[16:17], s4, v107
	v_writelane_b32 v10, s8, 12
	v_writelane_b32 v11, s9, 12
	v_cmp_le_u32_e64 s[8:9], s4, v108
	v_writelane_b32 v10, s12, 13
	v_writelane_b32 v11, s13, 13
	v_cmp_le_u32_e64 s[12:13], s4, v109
	v_writelane_b32 v10, s16, 14
	v_writelane_b32 v11, s17, 14
	v_cmp_le_u32_e64 s[16:17], s4, v110
	v_writelane_b32 v10, s8, 15
	v_writelane_b32 v11, s9, 15
	v_cmp_le_u32_e64 s[8:9], s4, v112
	v_writelane_b32 v10, s12, 16
	v_writelane_b32 v11, s13, 16
	v_cmp_le_u32_e64 s[12:13], s4, v114
	v_writelane_b32 v10, s16, 17
	v_writelane_b32 v11, s17, 17
	v_cmp_le_u32_e64 s[16:17], s4, v116
	v_writelane_b32 v10, s8, 18
	v_writelane_b32 v11, s9, 18
	v_cmp_le_u32_e64 s[8:9], s4, v118
	v_writelane_b32 v10, s12, 19
	v_writelane_b32 v11, s13, 19
	v_cmp_le_u32_e64 s[12:13], s4, v120
	v_writelane_b32 v10, s16, 20
	v_writelane_b32 v11, s17, 20
	v_cmp_le_u32_e64 s[16:17], s4, v122
	v_writelane_b32 v10, s8, 21
	v_writelane_b32 v11, s9, 21
	v_writelane_b32 v10, s12, 22
	v_writelane_b32 v11, s13, 22
	v_writelane_b32 v10, s16, 23
	v_writelane_b32 v11, s17, 23
	v_mov_b32_e32 v2, v10
	v_mov_b32_e32 v3, v11
	s_branch .LBB0_2681
.Ltk3_x16:
	v_cmp_le_u32_e64 s[8:9], s4, v93
	v_cmp_le_u32_e64 s[12:13], s4, v94
	v_cmp_le_u32_e64 s[16:17], s4, v95
	s_nop 0
	v_writelane_b32 v10, s8, 0
	v_writelane_b32 v11, s9, 0
	v_cmp_le_u32_e64 s[8:9], s4, v96
	v_writelane_b32 v10, s12, 1
	v_writelane_b32 v11, s13, 1
	v_cmp_le_u32_e64 s[12:13], s4, v97
	v_writelane_b32 v10, s16, 2
	v_writelane_b32 v11, s17, 2
	v_cmp_le_u32_e64 s[16:17], s4, v98
	v_writelane_b32 v10, s8, 3
	v_writelane_b32 v11, s9, 3
	v_cmp_le_u32_e64 s[8:9], s4, v99
	v_writelane_b32 v10, s12, 4
	v_writelane_b32 v11, s13, 4
	v_cmp_le_u32_e64 s[12:13], s4, v100
	v_writelane_b32 v10, s16, 5
	v_writelane_b32 v11, s17, 5
	v_cmp_le_u32_e64 s[16:17], s4, v101
	v_writelane_b32 v10, s8, 6
	v_writelane_b32 v11, s9, 6
	v_cmp_le_u32_e64 s[8:9], s4, v102
	v_writelane_b32 v10, s12, 7
	v_writelane_b32 v11, s13, 7
	v_cmp_le_u32_e64 s[12:13], s4, v103
	v_writelane_b32 v10, s16, 8
	v_writelane_b32 v11, s17, 8
	v_cmp_le_u32_e64 s[16:17], s4, v104
	v_writelane_b32 v10, s8, 9
	v_writelane_b32 v11, s9, 9
	v_cmp_le_u32_e64 s[8:9], s4, v105
	v_writelane_b32 v10, s12, 10
	v_writelane_b32 v11, s13, 10
	v_cmp_le_u32_e64 s[12:13], s4, v106
	v_writelane_b32 v10, s16, 11
	v_writelane_b32 v11, s17, 11
	v_cmp_le_u32_e64 s[16:17], s4, v107
	v_writelane_b32 v10, s8, 12
	v_writelane_b32 v11, s9, 12
	v_cmp_le_u32_e64 s[8:9], s4, v108
	v_writelane_b32 v10, s12, 13
	v_writelane_b32 v11, s13, 13
	v_writelane_b32 v10, s16, 14
	v_writelane_b32 v11, s17, 14
	v_writelane_b32 v10, s8, 15
	v_writelane_b32 v11, s9, 15
	v_mov_b32_e32 v2, v10
	v_mov_b32_e32 v3, v11
	s_branch .LBB0_2681
.Ltk3_x8:
	v_cmp_le_u32_e64 s[8:9], s4, v93
	v_cmp_le_u32_e64 s[12:13], s4, v94
	v_cmp_le_u32_e64 s[16:17], s4, v95
	s_nop 0
	v_writelane_b32 v10, s8, 0
	v_writelane_b32 v11, s9, 0
	v_cmp_le_u32_e64 s[8:9], s4, v96
	v_writelane_b32 v10, s12, 1
	v_writelane_b32 v11, s13, 1
	v_cmp_le_u32_e64 s[12:13], s4, v97
	v_writelane_b32 v10, s16, 2
	v_writelane_b32 v11, s17, 2
	v_cmp_le_u32_e64 s[16:17], s4, v98
	v_writelane_b32 v10, s8, 3
	v_writelane_b32 v11, s9, 3
	v_cmp_le_u32_e64 s[8:9], s4, v99
	v_writelane_b32 v10, s12, 4
	v_writelane_b32 v11, s13, 4
	v_cmp_le_u32_e64 s[12:13], s4, v100
	v_writelane_b32 v10, s16, 5
	v_writelane_b32 v11, s17, 5
	v_writelane_b32 v10, s8, 6
	v_writelane_b32 v11, s9, 6
	v_writelane_b32 v10, s12, 7
	v_writelane_b32 v11, s13, 7
	v_mov_b32_e32 v2, v10
	v_mov_b32_e32 v3, v11
	s_branch .LBB0_2681
